# conversion LDS staging addresses precomputed per unit (v170/v171); V-piece m0 write hoisted above the MFMA
# baseline (speedup 1.0000x reference)
; DEVI int tidx() { int t = threadIdx.x; asm volatile("" : "+v"(t)); __builtin_assume(t >= 0 && t < 512); return t; }
; DEVI unsigned cvt_pk_bf16(float lo, float hi) { unsigned r; asm volatile("v_cvt_pk_bf16_f32 %0, %1, %2" : "=v"(r) : "v"(lo), "v"(hi)); return r; }
; DEVI float bf2f(bf16_t h) { return __uint_as_float(((unsigned)h) << 16); }
; DEVI void attn_unit8(const Params& p, char* smem, int unit, int l, int& cvs  , CvRun& crun) {
;     const int tid = tidx(), wid = __builtin_amdgcn_readfirstlane(tid >> 6), lane = tid & 63, r32 = lane & 31, hi = lane >> 5;
;     const int x8 = unit & 7, v8 = unit >> 3, bh = x8 + 8 * (v8 >> 4), qt = v8 & 15, b = bh >> 3, hh = bh & 7;
;     char* K_lds = smem; char* V_lds = smem + 73728;
;     float* wsx = (float*)(smem + 122880) + wid * 64; float* li_l = wsx; float* al_l = wsx + 32;
;     const bf16_t* Kg = p.kfull + (size_t)bh * S_ * 96; const bf16_t* Vg = p.vfull + (size_t)bh * S_ * 64;
;     const size_t qtok = (size_t)b * S_ + qt * 256 + wid * 32 + r32;
;     bf16x8 qr[6];
;     { const bf16_t* qp = p.qbuf + qtok * 768 + hh * 96 + hi * 8;
; #pragma unroll
;       for (int d0 = 0; d0 < 6; ++d0) qr[d0] = *(const bf16x8*)(qp + d0 * 16);
;       const f32x4 c0 = *(const f32x4*)(p.cs + qtok * 16 + hi * 8), c1 = *(const f32x4*)(p.cs + qtok * 16 + hi * 8 + 4);
;       const f32x4 s0 = *(const f32x4*)(p.sn + qtok * 16 + hi * 8), s1 = *(const f32x4*)(p.sn + qtok * 16 + hi * 8 + 4);
;       float o1[8], o2[8];
; #pragma unroll
;       for (int j = 0; j < 8; ++j) { const float x1 = bf2f((bf16_t)qr[4][j]), x2 = bf2f((bf16_t)qr[5][j]); const float cc = j < 4 ? c0[j] : c1[j - 4], ss = j < 4 ? s0[j] : s1[j - 4];
;           o1[j] = x1 * cc - x2 * ss; o2[j] = x2 * cc + x1 * ss; }
;       u32x4 w1, w2;
; #pragma unroll
;       for (int j = 0; j < 4; ++j) { w1[j] = cvt_pk_bf16(o1[2 * j], o1[2 * j + 1]); w2[j] = cvt_pk_bf16(o2[2 * j], o2[2 * j + 1]); }
;       qr[4] = *(bf16x8*)&w1; qr[5] = *(bf16x8*)&w2; }
.LBB0_665:
	v_mov_b32_e32 v86, v0
	s_ashr_i32 s5, s83, 4
	v_readfirstlane_b32 s4, v86
	s_lshr_b32 s53, s4, 6
	s_and_b32 s52, s5, -8
	s_and_b32 s8, s4, 0x3fffffc0
	s_load_dwordx4 s[4:7], s[24:25], 0x1a0
	s_load_dwordx4 s[12:15], s[24:25], 0x110
	s_and_b32 s87, s83, 7
	s_ashr_i32 s16, s83, 7
	s_lshl_b32 s8, s8, 2
	s_or_b32 s10, s52, s87
	s_add_i32 s91, s8, 0
	s_ashr_i32 s17, s16, 31
	s_lshl_b32 s8, s83, 5
	s_ashr_i32 s11, s10, 31
	s_lshl_b64 s[16:17], s[16:17], 12
	s_and_b32 s8, s8, 0xf00
	s_and_b32 s2, s62, 7
	s_add_i32 s91, s91, 0x1e000
	s_waitcnt lgkmcnt(0)
	v_mov_b32_e32 v2, s4
	v_mov_b32_e32 v3, s5
	s_lshl_b64 s[4:5], s[10:11], 19
	s_or_b32 s8, s16, s8
	s_lshl_b32 s11, s53, 5
	v_and_b32_e32 v176, 31, v86
	s_add_u32 s48, s8, s11
	v_or_b32_e32 v10, s48, v176
	s_movk_i32 s8, 0x600
	s_addc_u32 s49, s17, 0
	v_mad_u64_u32 v[2:3], s[16:17], v10, s8, v[2:3]
	v_bfe_u32 v186, v86, 5, 1
	v_mad_i32_i24 v3, s49, v177, v3
	s_mul_i32 s8, s87, 0xc0
	v_mov_b32_e32 v11, s49
	v_lshl_add_u64 v[2:3], v[2:3], 0, s[8:9]
	v_lshlrev_b32_e32 v178, 4, v186
	v_mov_b32_e32 v179, v175
	v_lshl_add_u64 v[26:27], v[2:3], 0, v[178:179]
	v_lshlrev_b64 v[10:11], 6, v[10:11]
	global_load_dwordx4 v[2:5], v[26:27], off offset:128
	global_load_dwordx4 v[6:9], v[26:27], off offset:160
	v_lshl_add_u64 v[12:13], s[12:13], 0, v[10:11]
	v_and_b32_e32 v174, 32, v86
	v_lshl_add_u64 v[10:11], s[14:15], 0, v[10:11]
	v_lshl_add_u64 v[22:23], v[12:13], 0, v[174:175]
	v_lshl_add_u64 v[18:19], v[10:11], 0, v[174:175]
	global_load_dwordx4 v[10:13], v[18:19], off
	global_load_dwordx4 v[14:17], v[22:23], off
	s_nop 0
	global_load_dwordx4 v[18:21], v[18:19], off offset:16
	s_nop 0
	global_load_dwordx4 v[22:25], v[22:23], off offset:16
	s_load_dwordx2 s[50:51], s[24:25], 0x1b0
	global_load_dwordx4 v[150:153], v[26:27], off
	global_load_dwordx4 v[138:141], v[26:27], off offset:32
	global_load_dwordx4 v[134:137], v[26:27], off offset:64
	global_load_dwordx4 v[130:133], v[26:27], off offset:96
	s_mul_hi_i32 s8, s10, 0xc0000
	s_mul_i32 s10, s10, 0xc0000
	s_add_u32 s10, s6, s10
	s_addc_u32 s11, s7, s8
	s_lshl_b32 s61, s53, 10
	s_add_i32 s96, s61, 0
	s_waitcnt lgkmcnt(0)
	s_add_u32 s4, s50, s4
	s_mov_b32 m0, s96
	v_lshlrev_b32_e32 v88, 6, v186
	s_addc_u32 s5, s51, s5
	s_add_i32 s97, s75, s61
	v_lshlrev_b32_e32 v90, 2, v86
	v_and_b32_e32 v91, 63, v86
	v_lshlrev_b32_e32 v93, 4, v91
	v_lshlrev_b32_e32 v92, 3, v91
	v_lshlrev_b32_e32 v94, 1, v91
	s_mov_b32 s8, s9
	s_mov_b32 s12, s9
	s_mov_b32 s13, s9
	s_mov_b32 s14, s9
	s_mov_b32 s15, s9
	s_mov_b32 s16, s9
	s_mov_b32 s17, s9
	s_mov_b32 s18, s9
	s_mov_b32 s19, s9
	s_mov_b32 s20, s9
	s_mov_b32 s21, s9
	s_mov_b32 s22, s9
	s_mov_b32 s23, s9
	s_mulk_i32 s53, 0x900
	v_mov_b32_e32 v83, v175
	v_mov_b32_e32 v85, v175
	v_and_b32_e32 v114, 28, v90
	v_lshl_add_u32 v187, v176, 2, s91
	v_mul_u32_u24_e32 v201, 0x44, v114
	v_bfe_u32 v195, v91, 1, 2
	v_mov_b32_e32 v207, 1.0
	s_mov_b32 s89, s9
	v_mov_b32_e32 v188, v175
	s_waitcnt vmcnt(9)
	v_lshlrev_b32_e32 v27, 16, v2
	s_waitcnt vmcnt(8)
	v_lshlrev_b32_e32 v26, 16, v6
	v_and_b32_e32 v33, 0xffff0000, v2
	v_lshlrev_b32_e32 v35, 16, v3
	s_waitcnt vmcnt(7)
	v_mov_b32_e32 v28, v10
	s_waitcnt vmcnt(6)
	v_mov_b32_e32 v29, v14
	v_mov_b32_e32 v36, v12
	v_mov_b32_e32 v37, v16
	v_mov_b32_e32 v38, v16
	v_mov_b32_e32 v39, v12
	v_and_b32_e32 v3, 0xffff0000, v3
	v_and_b32_e32 v2, 0xffff0000, v7
	v_mov_b32_e32 v16, v13
	v_mov_b32_e32 v12, v17
	v_and_b32_e32 v32, 0xffff0000, v6
	v_lshlrev_b32_e32 v34, 16, v7
	v_pk_mul_f32 v[6:7], v[28:29], v[26:27]
	v_pk_mul_f32 v[16:17], v[16:17], v[2:3]
	v_pk_mul_f32 v[2:3], v[12:13], v[2:3]
	v_mov_b32_e32 v30, v14
	v_mov_b32_e32 v31, v10
	v_sub_f32_e32 v12, v7, v6
	v_sub_f32_e32 v16, v17, v16
	v_add_f32_e32 v17, v2, v3
	v_lshlrev_b32_e32 v3, 16, v4
	v_lshlrev_b32_e32 v2, 16, v8
	s_waitcnt vmcnt(5)
	v_mov_b32_e32 v6, v18
	s_waitcnt vmcnt(4)
	v_mov_b32_e32 v7, v22
	v_pk_mul_f32 v[26:27], v[30:31], v[26:27]
	v_pk_mul_f32 v[6:7], v[6:7], v[2:3]
	v_add_f32_e32 v13, v26, v27
	v_sub_f32_e32 v26, v7, v6
	v_mov_b32_e32 v6, v22
	v_mov_b32_e32 v7, v18
	v_pk_mul_f32 v[2:3], v[6:7], v[2:3]
	v_mov_b32_e32 v22, v19
	v_add_f32_e32 v27, v2, v3
	v_and_b32_e32 v3, 0xffff0000, v4
	v_and_b32_e32 v2, 0xffff0000, v8
	v_mov_b32_e32 v18, v23
	v_pk_mul_f32 v[6:7], v[22:23], v[2:3]
	v_pk_mul_f32 v[2:3], v[18:19], v[2:3]
	v_sub_f32_e32 v8, v7, v6
	v_add_f32_e32 v18, v2, v3
	v_lshlrev_b32_e32 v3, 16, v5
	v_lshlrev_b32_e32 v2, 16, v9
	v_mov_b32_e32 v6, v20
	v_mov_b32_e32 v7, v24
	v_pk_mul_f32 v[6:7], v[6:7], v[2:3]
	v_mov_b32_e32 v14, v11
	v_sub_f32_e32 v19, v7, v6
	v_mov_b32_e32 v6, v24
	v_mov_b32_e32 v7, v20
	v_pk_mul_f32 v[2:3], v[6:7], v[2:3]
	v_mov_b32_e32 v24, v21
	v_add_f32_e32 v6, v2, v3
	v_and_b32_e32 v3, 0xffff0000, v5
	v_and_b32_e32 v2, 0xffff0000, v9
	v_mov_b32_e32 v20, v25
	v_mov_b32_e32 v10, v15
	v_pk_mul_f32 v[4:5], v[24:25], v[2:3]
	v_pk_mul_f32 v[2:3], v[20:21], v[2:3]
	v_pk_mul_f32 v[14:15], v[14:15], v[32:33]
	v_pk_mul_f32 v[10:11], v[10:11], v[32:33]
	v_pk_mul_f32 v[28:29], v[36:37], v[34:35]
	v_pk_mul_f32 v[30:31], v[38:39], v[34:35]
	v_add_f32_e32 v2, v2, v3
	v_sub_f32_e32 v14, v15, v14
	v_add_f32_e32 v10, v10, v11
	v_sub_f32_e32 v11, v29, v28
	v_add_f32_e32 v15, v30, v31
	v_sub_f32_e32 v4, v5, v4
	v_cvt_pk_bf16_f32 v146, v12, v14
	v_cvt_pk_bf16_f32 v142, v13, v10
	v_cvt_pk_bf16_f32 v147, v11, v16
	v_cvt_pk_bf16_f32 v143, v15, v17
	v_cvt_pk_bf16_f32 v148, v26, v8
	v_cvt_pk_bf16_f32 v144, v27, v18
	v_cvt_pk_bf16_f32 v149, v19, v4
	v_cvt_pk_bf16_f32 v145, v6, v2
	v_mul_u32_u24_e32 v2, 0xaaab, v86
	v_lshrrev_b32_e32 v3, 19, v2
	v_mul_lo_u16_e32 v4, 12, v3
	v_sub_u16_e32 v4, v86, v4
	v_lshrrev_b32_e32 v2, 21, v2
; #define LAS __attribute__((address_space(3)))
; DEVI int v_rd_base(int lane) { return ((lane & 3) << 3) | (((lane >> 2) & 3) << 6) | (((lane >> 4) & 1) << 5) | (((lane >> 5) & 1) << 8); }
; #define VM0() asm volatile("s_waitcnt vmcnt(0)" ::: "memory")
; DEVI void attn_unit8(const Params& p, char* smem, int unit, int l, int& cvs  , CvRun& crun) {
;     ...
;     int ksrc[3];
; #pragma unroll
;     for (int i = 0; i < 3; ++i) { const int pc = tid + 512 * i, row = pc / 12, ch = (pc % 12) ^ ((row >> 2) & 3); ksrc[i] = row * 192 + ch * 16; }
;     const int vsrc = wid * 1024 + ((lane >> 2) & 7) * 128 + (lane >> 5) * 64 + (lane & 3) * 16;
;     LAS char* const Kl = (LAS char*)K_lds + wid * 1024; LAS char* const Vl = (LAS char*)V_lds + wid * 1024;
;     ...
;     const int vb0 = (int)(uintptr_t)(LAS char*)V_lds + v_rd_base(lane);
;     float m_reg = 0.f, l_reg = 0.f; f32x16 o[2];
; #pragma unroll
;     for (int d = 0; d < 2; ++d)
; #pragma unroll
;         for (int r = 0; r < 16; ++r) o[d][r] = 0.f;
;     f32x16 pA0, pA1, pB0, pB1; float alA, alB; bf16x8 pa0, pa1, pa2, pa3;
;     constexpr int NTILE = S_ / 128;
;     B_DMA(0, 0); B_DMA(1, 1); VM0(); __syncthreads();
	v_bitop3_b32 v2, v2, v4, 3 bitop3:0x6c
	v_mul_u32_u24_e32 v3, 0xc0, v3
	v_lshl_add_u32 v174, v2, 4, v3
	v_or_b32_e32 v2, 0x200, v86
	v_mul_u32_u24_sdwa v3, v2, s74 dst_sel:DWORD dst_unused:UNUSED_PAD src0_sel:WORD_0 src1_sel:DWORD
	v_lshrrev_b32_e32 v4, 19, v3
	v_mul_lo_u16_e32 v5, 12, v4
	v_sub_u16_e32 v2, v2, v5
	v_lshrrev_b32_e32 v3, 21, v3
	v_bitop3_b32 v2, v3, v2, 3 bitop3:0x6c
	v_mul_u32_u24_e32 v3, 0xc0, v4
	v_lshl_add_u32 v82, v2, 4, v3
	v_or_b32_e32 v2, 0x400, v86
	v_mul_u32_u24_sdwa v3, v2, s74 dst_sel:DWORD dst_unused:UNUSED_PAD src0_sel:WORD_0 src1_sel:DWORD
	v_lshrrev_b32_e32 v4, 19, v3
	v_mul_lo_u16_e32 v5, 12, v4
	v_sub_u16_e32 v2, v2, v5
	v_lshrrev_b32_e32 v3, 21, v3
	v_bitop3_b32 v2, v3, v2, 3 bitop3:0x6c
	v_mul_u32_u24_e32 v3, 0xc0, v4
	v_lshl_add_u32 v84, v2, 4, v3
	v_lshlrev_b32_e32 v2, 5, v86
	v_and_b32_e32 v87, 0x380, v2
	v_lshlrev_b32_e32 v3, 4, v86
	global_load_lds_dwordx4 v174, s[10:11]
	s_add_i32 m0, s96, 0x2000
	v_or_b32_e32 v2, v88, v87
	v_and_b32_e32 v89, 48, v3
	global_load_lds_dwordx4 v82, s[10:11]
	s_add_i32 m0, s96, 0x4000
	v_or3_b32 v2, v2, v89, s61
	global_load_lds_dwordx4 v84, s[10:11]
	v_mov_b32_e32 v3, v175
	s_mov_b32 m0, s97
	v_lshl_add_u64 v[4:5], s[4:5], 0, v[2:3]
	global_load_lds_dwordx4 v2, s[4:5]
	s_add_i32 m0, s97, 0x2000
	s_mov_b64 s[72:73], 0x2000
	v_lshl_add_u64 v[2:3], v[4:5], 0, s[72:73]
	s_add_u32 s4, s10, 0x6000
	global_load_lds_dwordx4 v[2:3], off
	s_addc_u32 s5, s11, 0
	s_add_i32 m0, s96, 0x6000
	v_lshl_add_u64 v[2:3], v[4:5], 0, s[44:45]
	global_load_lds_dwordx4 v174, s[4:5]
	s_add_i32 m0, s96, 0x8000
	v_mul_u32_u24_e32 v10, 0xc0, v176
	global_load_lds_dwordx4 v82, s[4:5]
	s_add_i32 m0, s96, 0xa000
	v_and_b32_e32 v11, 48, v90
	global_load_lds_dwordx4 v84, s[4:5]
	s_add_i32 m0, s97, 0x4000
	v_bitop3_b32 v129, v178, v10, v11 bitop3:0xde
	global_load_lds_dwordx4 v[2:3], off
	v_lshl_add_u64 v[2:3], v[4:5], 0, s[42:43]
	s_add_i32 m0, s97, 0x6000
	v_add_u32_e32 v189, 0, v129
	global_load_lds_dwordx4 v[2:3], off
	s_waitcnt vmcnt(0)
	s_waitcnt vmcnt(0) lgkmcnt(0)
	s_barrier
; template <bool FIRST> DEVI bool partialSM(f32x16& p0, f32x16& p1, float& m_reg, float& alpha) {
;     float pmax = p0[0];
; #pragma unroll
;     for (int r = 1; r < 16; ++r) pmax = fmaxf(pmax, p0[r]);
; #pragma unroll
;     for (int r = 0; r < 16; ++r) pmax = fmaxf(pmax, p1[r]);
;     { auto rr = __builtin_amdgcn_permlane32_swap(__float_as_uint(pmax), __float_as_uint(pmax), false, false);
;       pmax = fmaxf(__uint_as_float(rr[0]), __uint_as_float(rr[1])); }
;     if (FIRST) { m_reg = pmax; alpha = 1.f;
; #pragma unroll
;         for (int r = 0; r < 16; ++r) { p0[r] = __builtin_amdgcn_exp2f(p0[r] - pmax); p1[r] = p1[r] - pmax; }
;         return false;
; DEVI void qkt(f32x16& p0, f32x16& p1, const char* Kb, const bf16x8 (&qr)[6], int r32, int hi, const f32x16& cinit) {
; #pragma unroll
;     for (int d0 = 0; d0 < 6; ++d0) { const int cb = (d0 * 16 + hi * 8) * 2;
;         const bf16x8 k0 = *(const bf16x8*)(Kb + KSWZ(r32, cb)), k1 = *(const bf16x8*)(Kb + KSWZ(32 + r32, cb));
;         p0 = __builtin_amdgcn_mfma_f32_32x32x16_bf16(k0, qr[d0], d0 == 0 ? cinit : p0, 0, 0, 0);
;         p1 = __builtin_amdgcn_mfma_f32_32x32x16_bf16(k1, qr[d0], d0 == 0 ? cinit : p1, 0, 0, 0); }
; }
	ds_read_b128 v[2:5], v189
	ds_read_b128 v[6:9], v189 offset:6144
	s_waitcnt lgkmcnt(1)
	v_mfma_f32_32x32x16_bf16 v[34:49], v[2:5], v[150:153], 0
	v_or_b32_e32 v2, 32, v178
	v_bitop3_b32 v184, v2, v10, v11 bitop3:0xde
	v_add_u32_e32 v190, 0, v184
	s_mov_b32 s10, s9
	s_mov_b32 s11, s9
	s_lshl_b32 s71, s54, 5
	s_lshl_b32 s84, s54, 4
	s_waitcnt lgkmcnt(0)
	v_mfma_f32_32x32x16_bf16 v[18:33], v[6:9], v[150:153], 0
	ds_read_b128 v[2:5], v190
	ds_read_b128 v[6:9], v190 offset:6144
	s_lshl_b32 s85, s54, 3
	s_lshl_b32 s88, s54, 1
	v_cmp_gt_u32_e64 s[4:5], 32, v91
	s_waitcnt lgkmcnt(1)
	v_mfma_f32_32x32x16_bf16 v[34:49], v[2:5], v[138:141], v[34:49]
	v_or_b32_e32 v2, 64, v178
	v_xad_u32 v185, v2, v11, v10
	v_add_u32_e32 v191, 0, v185
	s_waitcnt lgkmcnt(0)
	v_mfma_f32_32x32x16_bf16 v[18:33], v[6:9], v[138:141], v[18:33]
	ds_read_b128 v[2:5], v191
	ds_read_b128 v[6:9], v191 offset:6144
	s_waitcnt lgkmcnt(1)
	v_mfma_f32_32x32x16_bf16 v[34:49], v[2:5], v[134:137], v[34:49]
	v_or_b32_e32 v2, 0x60, v178
	v_xad_u32 v204, v2, v11, v10
	v_add_u32_e32 v192, 0, v204
	ds_read_b128 v[2:5], v192
	s_waitcnt lgkmcnt(1)
	v_mfma_f32_32x32x16_bf16 v[18:33], v[6:9], v[134:137], v[18:33]
	ds_read_b128 v[6:9], v192 offset:6144
	s_waitcnt lgkmcnt(1)
	v_mfma_f32_32x32x16_bf16 v[34:49], v[2:5], v[130:133], v[34:49]
	v_and_b32_e32 v2, 0xc0, v93
	v_and_or_b32 v12, v92, 24, v2
	v_or_b32_e32 v2, 0x80, v178
	v_xad_u32 v205, v2, v11, v10
	v_add_u32_e32 v193, 0, v205
	ds_read_b128 v[2:5], v193
	s_waitcnt lgkmcnt(1)
	v_mfma_f32_32x32x16_bf16 v[18:33], v[6:9], v[130:133], v[18:33]
	v_and_b32_e32 v6, 32, v94
	v_and_b32_e32 v7, 0x100, v92
	v_or3_b32 v179, v12, v6, v7
	ds_read_b128 v[6:9], v193 offset:6144
	v_add_u32_e32 v115, s75, v179
	s_waitcnt lgkmcnt(1)
	v_mfma_f32_32x32x16_bf16 v[34:49], v[2:5], v[146:149], v[34:49]
	v_or_b32_e32 v2, 0xa0, v178
	v_xad_u32 v206, v2, v11, v10
	v_add_u32_e32 v194, 0, v206
	ds_read_b128 v[2:5], v194
	ds_read_b128 v[50:53], v194 offset:6144
	s_waitcnt lgkmcnt(2)
	v_mfma_f32_32x32x16_bf16 v[18:33], v[6:9], v[146:149], v[18:33]
	s_waitcnt lgkmcnt(1)
	v_mfma_f32_32x32x16_bf16 v[34:49], v[2:5], v[142:145], v[34:49]
	v_mov_b64_e32 v[2:3], s[8:9]
	v_mov_b64_e32 v[4:5], s[10:11]
	v_mov_b64_e32 v[6:7], s[12:13]
	v_mov_b64_e32 v[8:9], s[14:15]
	v_mov_b64_e32 v[10:11], s[16:17]
	v_mov_b64_e32 v[12:13], s[18:19]
	v_mov_b64_e32 v[14:15], s[20:21]
	s_waitcnt lgkmcnt(0)
	v_mfma_f32_32x32x16_bf16 v[18:33], v[50:53], v[142:145], v[18:33]
	s_nop 2
	v_max_f32_e32 v50, v35, v35
	v_max_f32_e32 v51, v34, v34
	v_max_f32_e32 v50, v51, v50
	v_max3_f32 v50, v50, v36, v37
	v_max3_f32 v50, v50, v38, v39
	v_max3_f32 v50, v50, v40, v41
	v_max3_f32 v50, v50, v42, v43
	v_max3_f32 v50, v50, v44, v45
	v_max3_f32 v50, v50, v46, v47
	v_max3_f32 v50, v50, v48, v49
	v_max3_f32 v50, v50, v18, v19
	v_max3_f32 v50, v50, v20, v21
	v_max3_f32 v50, v50, v22, v23
	v_max3_f32 v50, v50, v24, v25
	v_max3_f32 v50, v50, v26, v27
	v_max3_f32 v50, v50, v28, v29
	v_max3_f32 v50, v50, v30, v31
	v_max3_f32 v50, v50, v32, v33
	v_mov_b32_e32 v51, v50
	s_nop 1
	v_permlane32_swap_b32_e32 v50, v51
	v_max_f32_e32 v51, v51, v51
	v_max_f32_e32 v50, v50, v50
	v_max_f32_e32 v203, v50, v51
	v_sub_f32_e32 v34, v34, v203
	v_exp_f32_e32 v50, v34
	v_sub_f32_e32 v34, v35, v203
	v_exp_f32_e32 v51, v34
	v_sub_f32_e32 v34, v36, v203
	v_exp_f32_e32 v52, v34
	v_sub_f32_e32 v34, v37, v203
	v_exp_f32_e32 v53, v34
	v_sub_f32_e32 v34, v38, v203
	v_exp_f32_e32 v54, v34
	v_sub_f32_e32 v34, v39, v203
	v_exp_f32_e32 v55, v34
	v_sub_f32_e32 v34, v40, v203
	v_exp_f32_e32 v56, v34
	v_sub_f32_e32 v34, v41, v203
	v_exp_f32_e32 v57, v34
	v_sub_f32_e32 v34, v42, v203
	v_mov_b64_e32 v[16:17], s[22:23]
	v_exp_f32_e32 v58, v34
	v_sub_f32_e32 v34, v43, v203
	v_sub_f32_e32 v67, v19, v203
	s_add_i32 s8, s53, 0
	v_bfe_u32 v19, v86, 1, 5
	v_exp_f32_e32 v59, v34
	v_sub_f32_e32 v34, v44, v203
	v_sub_f32_e32 v68, v20, v203
	s_add_i32 s8, s8, 0x1e800
	v_and_b32_e32 v20, 28, v19
	s_or_b32 s10, s52, s2
	v_exp_f32_e32 v60, v34
	v_sub_f32_e32 v34, v45, v203
	v_sub_f32_e32 v69, v21, v203
	v_add_u32_e32 v200, s8, v20
	v_mov_b32_e32 v21, s8
	s_lshl_b32 s8, s54, 10
	s_ashr_i32 s11, s10, 31
	v_exp_f32_e32 v61, v34
	v_sub_f32_e32 v34, v46, v203
	s_add_i32 s70, s8, 0xf7f80000
	s_lshl_b64 s[12:13], s[10:11], 19
	v_exp_f32_e32 v62, v34
	v_sub_f32_e32 v34, v47, v203
	v_sub_f32_e32 v66, v18, v203
	v_lshrrev_b32_e32 v18, 2, v86
	s_add_u32 s12, s50, s12
	v_exp_f32_e32 v63, v34
	v_sub_f32_e32 v34, v48, v203
	v_sub_f32_e32 v70, v22, v203
	v_and_b32_e32 v128, 14, v18
	v_lshrrev_b32_e32 v22, 3, v86
	v_and_b32_e32 v18, 12, v18
	s_addc_u32 s13, s51, s13
	s_mul_i32 s8, s10, 0xc0000
	v_exp_f32_e32 v64, v34
	v_sub_f32_e32 v34, v49, v203
	v_mad_u32_u24 v198, v19, s77, v21
	v_and_b32_e32 v19, 0x80, v92
	v_and_b32_e32 v21, 16, v94
	v_and_b32_e32 v22, 4, v22
	v_and_or_b32 v197, v93, s76, v18
	v_or_b32_e32 v18, s61, v87
	s_mul_hi_i32 s2, s10, 0xc0000
	s_add_u32 s6, s6, s8
	v_exp_f32_e32 v65, v34
	v_or3_b32 v196, v19, v22, v21
	v_or3_b32 v18, v18, v88, v89
	v_mov_b32_e32 v19, v175
	s_addc_u32 s2, s7, s2
	v_and_b32_e32 v20, 1, v86

; DEVI unsigned cvt_pk_bf16(float lo, float hi) { unsigned r; asm volatile("v_cvt_pk_bf16_f32 %0, %1, %2" : "=v"(r) : "v"(lo), "v"(hi)); return r; }
; #define C_SPLAT() do { _Pragma("unroll") for (int _r = 0; _r < 16; ++_r) cinit[_r] = -m_reg; asm volatile("" : "+v"(cinit)); } while (0)
; DEVI void cv_finish(char* img  , int lane, const CvRegs& R) {
;     ...
;     const int n4 = (lane & 7) * 4, kq = lane >> 3;
;     const float sc = R.c.perm ? 16.f : 1.f;
; #pragma unroll
;     for (int c = 0; c < 4; ++c) { *(unsigned*)(img + (n4 + c) * 68 + (2 * kq) * 2) = cvt_pk_bf16(R.a0[c] * sc, R.b0[c] * sc); *(unsigned*)(img + (n4 + c) * 68 + (2 * kq + 16) * 2) = cvt_pk_bf16(R.a1[c] * sc, R.b1[c] * sc); }
;     asm volatile("" ::: "memory"); __builtin_amdgcn_wave_barrier();
;     const int n = lane >> 1, half = lane & 1; u32x4 w0, w1;
; #pragma unroll
;     for (int j = 0; j < 4; ++j) { w0[j] = *(const unsigned*)(img + n * 68 + half * 32 + j * 4); w1[j] = *(const unsigned*)(img + n * 68 + half * 32 + 16 + j * 4); }
; DEVI void attn_unit8(const Params& p, char* smem, int unit, int l, int& cvs  , CvRun& crun) {
;     ...
;     { f32x16 z; _Pragma("unroll") for (int r = 0; r < 16; ++r) z[r] = 0.f;
;       qkt(pA0, pA1, K_lds, qr, r32, hi, z); } partialSM<true>(pA0, pA1, m_reg, alA); C_SPLAT();
;     int s0 = 0, s1 = 1, s2 = 2;
	s_add_u32 s6, s6, 0xc000
	v_xor_b32_e32 v34, 0x80000000, v203
	v_sub_f32_e32 v81, v33, v203
	v_sub_f32_e32 v80, v32, v203
	v_sub_f32_e32 v79, v31, v203
	v_sub_f32_e32 v78, v30, v203
	v_sub_f32_e32 v77, v29, v203
	v_sub_f32_e32 v76, v28, v203
	v_sub_f32_e32 v75, v27, v203
	v_sub_f32_e32 v74, v26, v203
	v_sub_f32_e32 v73, v25, v203
	v_sub_f32_e32 v72, v24, v203
	v_sub_f32_e32 v71, v23, v203
	v_lshlrev_b32_e32 v199, 5, v20
	v_lshlrev_b32_e32 v180, 4, v20
	v_mov_b32_e32 v116, v18
	v_add_u32_e32 v117, 0x2000, v18
	s_addc_u32 s7, s2, 0
	s_add_u32 s44, s12, 0x8000
	s_addc_u32 s45, s13, 0
	v_mov_b64_e32 v[32:33], v[16:17]
	v_mov_b32_e32 v35, v34
	v_mov_b32_e32 v36, v34
	v_mov_b32_e32 v37, v34
	v_mov_b32_e32 v38, v34
	v_mov_b32_e32 v39, v34
	v_mov_b32_e32 v40, v34
	v_mov_b32_e32 v41, v34
	v_mov_b32_e32 v42, v34
	v_mov_b32_e32 v43, v34
	v_mov_b32_e32 v44, v34
	v_mov_b32_e32 v45, v34
	v_mov_b32_e32 v46, v34
	v_mov_b32_e32 v47, v34
	v_mov_b32_e32 v48, v34
	v_mov_b32_e32 v49, v34
	v_mov_b32_e32 v118, v174
	v_mov_b32_e32 v120, v82
	v_mov_b32_e32 v122, v84
	s_mov_b64 s[12:13], s[6:7]
	s_add_u32 s67, s6, 0xb4000
	v_add_u32_e32 v170, v200, v201
	v_add_u32_e32 v171, v198, v199
	v_mov_b64_e32 v[30:31], v[14:15]
	v_mov_b64_e32 v[28:29], v[12:13]
	v_mov_b64_e32 v[26:27], v[10:11]
	v_mov_b64_e32 v[24:25], v[8:9]
	v_mov_b64_e32 v[22:23], v[6:7]
	v_mov_b64_e32 v[20:21], v[4:5]
	v_mov_b64_e32 v[18:19], v[2:3]
	s_mov_b32 s6, 2
	s_mov_b32 s2, 1

; DEVI f32x4 ld_nt(const float* p) { return __builtin_nontemporal_load((const f32x4*)p); }
; DEVI void cv_next(const Params& p, int l, int s, int lane, int stride, CvRun& run) {
;     ...
;     run.c = cv_slice(p, l, s, lane); run.left = 0;
;     if ((stride & 511) == 0) {
;         if (s < NS_W13) { const int e = s >> 9, es = stride >> 9; if (e < NE) { run.left = (NE - 1 - e) / es; run.sstep = (long)es * 1024 * 256; run.dstep = (long)es * 512 * 1024; } }
;         else { const int e = (s - NS_W13) >> 8, es = stride >> 8; if (e < NE) { run.left = (NE - 1 - e) / es; run.sstep = (long)es * 256 * 1024; run.dstep = (long)es * 1024 * 256; } } }
; }
; DEVI void cv_issue(const Params& p, int l, int s, int lane, CvRegs& R, CvRun& run) {
;     R.live = s < NS_SLICES ? 1 : 0;
;     if (R.live) { cv_next(p, l, s, lane, (int)gridDim.x * 8, run); R.c = run.c; const int kq = lane >> 3;
;         const float* sp = R.c.src + (size_t)(R.c.k0 + 2 * kq) * R.c.ld;
;         R.a0 = ld_nt(sp); R.b0 = ld_nt(sp + R.c.ld); R.a1 = ld_nt(sp + (size_t)16 * R.c.ld); R.b1 = ld_nt(sp + (size_t)17 * R.c.ld); }
.LBB0_695:
	v_add_u32_e32 v252, s10, v128
	s_mov_b64 s[68:69], s[18:19]
	s_mov_b64 s[40:41], s[20:21]
	v_mul_lo_u32 v243, v252, s6
	v_lshlrev_b32_e32 v242, 2, v114
	s_lshl_b32 s72, s6, 2
	s_lshl_b32 s73, s6, 6
	v_lshl_add_u32 v242, v243, 2, v242
	v_add_u32_e32 v243, s72, v242
	v_add_u32_e32 v244, s73, v242
	v_add_u32_e32 v245, s73, v243
	s_cmp_eq_u32 s95, 0
	s_cselect_b64 s[72:73], -1, 0
	v_cndmask_b32_e64 v246, v196, v197, s[72:73]
	v_or_b32_e32 v246, v246, v195
	v_add_u32_e32 v246, s8, v246
	v_mul_lo_u32 v246, v246, s94
	v_add3_u32 v246, v246, v180, s10
	v_lshlrev_b32_e32 v246, 1, v246
	v_mov_b32_e32 v247, 0
	s_ashr_i32 s7, s6, 31
	v_mad_i64_i32 v[252:253], s[16:17], v252, s6, 0
	v_lshl_add_u64 v[252:253], v[252:253], 2, v[250:251]
	s_lshl_b64 s[16:17], s[6:7], 2
	v_lshl_add_u64 v[254:255], v[252:253], 0, s[16:17]
	global_load_dwordx4 v[154:157], v[252:253], off nt
	global_load_dwordx4 v[158:161], v[254:255], off nt
	v_mad_i64_i32 v[252:253], s[18:19], s6, 60, v[254:255]
	v_lshl_add_u64 v[254:255], v[252:253], 0, s[16:17]
	global_load_dwordx4 v[162:165], v[252:253], off nt
	global_load_dwordx4 v[166:169], v[254:255], off nt
	s_mov_b64 s[26:27], s[22:23]
	s_mov_b64 s[28:29], s[50:51]
	s_mov_b32 s56, s11
	s_mov_b32 s55, s95

; DEVI void cv_next(const Params& p, int l, int s, int lane, int stride, CvRun& run) {
;     ...
;     run.c = cv_slice(p, l, s, lane); run.left = 0;
;     if ((stride & 511) == 0) {
;         if (s < NS_W13) { const int e = s >> 9, es = stride >> 9; if (e < NE) { run.left = (NE - 1 - e) / es; run.sstep = (long)es * 1024 * 256; run.dstep = (long)es * 512 * 1024; } }
;         else { const int e = (s - NS_W13) >> 8, es = stride >> 8; if (e < NE) { run.left = (NE - 1 - e) / es; run.sstep = (long)es * 256 * 1024; run.dstep = (long)es * 1024 * 256; } } }
; }
	s_mov_b32 s57, s6
	s_mov_b32 s58, s10
	v_mov_b64_e32 v[172:173], v[182:183]
	s_mov_b32 s59, s94
	s_mov_b32 s60, s8

; DEVI void attn_unit8(const Params& p, char* smem, int unit, int l, int& cvs  , CvRun& crun) {
;     ...
;     for (int T = 0; T + 1 < NTILE; ++T) {
;         const char* Kb = K_lds + s0 * 24576; const int vb = vb0 + s0 * 16384;
;     ...
;         if (T + 2 < NTILE) B_DMA(T + 2, s2);
.LBB0_702:
	s_mul_i32 s98, s2, 0x6000
	s_add_i32 s98, s96, s98
	s_lshl_b32 s99, s2, 14
	s_add_i32 s99, s97, s99
	s_mul_i32 s6, s61, 0x6000
	s_add_i32 s6, s6, 0
	v_add_u32_e32 v249, s6, v129

; DEVI void qkt(f32x16& p0, f32x16& p1, const char* Kb, const bf16x8 (&qr)[6], int r32, int hi, const f32x16& cinit) {
; #pragma unroll
;     for (int d0 = 0; d0 < 6; ++d0) { const int cb = (d0 * 16 + hi * 8) * 2;
;         const bf16x8 k0 = *(const bf16x8*)(Kb + KSWZ(r32, cb)), k1 = *(const bf16x8*)(Kb + KSWZ(32 + r32, cb));
;         p0 = __builtin_amdgcn_mfma_f32_32x32x16_bf16(k0, qr[d0], d0 == 0 ? cinit : p0, 0, 0, 0);
;         p1 = __builtin_amdgcn_mfma_f32_32x32x16_bf16(k1, qr[d0], d0 == 0 ? cinit : p1, 0, 0, 0); }
; }
	s_mov_b32 m0, s98
	s_barrier
	ds_read_b128 v[234:237], v249
	ds_read_b128 v[210:213], v249 offset:6144
	global_load_lds_dwordx4 v118, s[12:13]
	s_waitcnt lgkmcnt(1)
	v_mfma_f32_32x32x16_bf16 v[98:113], v[234:237], v[150:153], v[34:49]
	s_add_i32 m0, s98, 0x2000

; DEVI void qkt(f32x16& p0, f32x16& p1, const char* Kb, const bf16x8 (&qr)[6], int r32, int hi, const f32x16& cinit) {
; #pragma unroll
;     for (int d0 = 0; d0 < 6; ++d0) { const int cb = (d0 * 16 + hi * 8) * 2;
;         const bf16x8 k0 = *(const bf16x8*)(Kb + KSWZ(r32, cb)), k1 = *(const bf16x8*)(Kb + KSWZ(32 + r32, cb));
;         p0 = __builtin_amdgcn_mfma_f32_32x32x16_bf16(k0, qr[d0], d0 == 0 ? cinit : p0, 0, 0, 0);
;         p1 = __builtin_amdgcn_mfma_f32_32x32x16_bf16(k1, qr[d0], d0 == 0 ? cinit : p1, 0, 0, 0); }
; }
	v_add_u32_e32 v126, s6, v184
	global_load_lds_dwordx4 v120, s[12:13]
	s_waitcnt lgkmcnt(0)
	v_mfma_f32_32x32x16_bf16 v[66:81], v[210:213], v[150:153], v[34:49]
	ds_read_b128 v[210:213], v126
	ds_read_b128 v[214:217], v126 offset:6144
	s_add_i32 m0, s98, 0x4000

; DEVI void qkt(f32x16& p0, f32x16& p1, const char* Kb, const bf16x8 (&qr)[6], int r32, int hi, const f32x16& cinit) {
; #pragma unroll
;     for (int d0 = 0; d0 < 6; ++d0) { const int cb = (d0 * 16 + hi * 8) * 2;
;         const bf16x8 k0 = *(const bf16x8*)(Kb + KSWZ(r32, cb)), k1 = *(const bf16x8*)(Kb + KSWZ(32 + r32, cb));
;         p0 = __builtin_amdgcn_mfma_f32_32x32x16_bf16(k0, qr[d0], d0 == 0 ? cinit : p0, 0, 0, 0);
;         p1 = __builtin_amdgcn_mfma_f32_32x32x16_bf16(k1, qr[d0], d0 == 0 ? cinit : p1, 0, 0, 0); }
; }
	v_add_u32_e32 v126, s6, v185
	global_load_lds_dwordx4 v122, s[12:13]
	s_mov_b32 m0, s99
	s_waitcnt lgkmcnt(1)
	v_mfma_f32_32x32x16_bf16 v[98:113], v[210:213], v[138:141], v[98:113]


	global_load_lds_dwordx4 v116, s[44:45]
	s_add_i32 m0, s99, 0x2000


; template <int OFF> DEVI s16x4 tr_read(int vb) { s16x4 r; asm volatile("ds_read_b64_tr_b16 %0, %1 offset:%2" : "=&v"(r) : "v"(vb), "i"(OFF) : "memory"); return r; }
; #define SBAR() __builtin_amdgcn_sched_barrier(0)
; #define PK4(P, BASE, OUT) do { u32x4 w = {cvt_pk_bf16(P[BASE + 0], P[BASE + 1]), cvt_pk_bf16(P[BASE + 2], P[BASE + 3]), cvt_pk_bf16(P[BASE + 4], P[BASE + 5]), cvt_pk_bf16(P[BASE + 6], P[BASE + 7])}; \
;     OUT = *reinterpret_cast<bf16x8*>(&w); } while (0)
; DEVI void pv_both(f32x16& o0, f32x16& o1, int vb, bf16x8 pa0, bf16x8 pa1, bf16x8 pa2, bf16x8 pa3) {
;     const s16x4 a0 = tr_read<v_rd_off(0, 0, 0)>(vb), b0 = tr_read<v_rd_off(0, 0, 1)>(vb), a1 = tr_read<v_rd_off(0, 1, 0)>(vb), b1 = tr_read<v_rd_off(0, 1, 1)>(vb);
;     const s16x4 a2 = tr_read<v_rd_off(0, 2, 0)>(vb), b2 = tr_read<v_rd_off(0, 2, 1)>(vb), a3 = tr_read<v_rd_off(0, 3, 0)>(vb), b3 = tr_read<v_rd_off(0, 3, 1)>(vb);
;     const s16x4 c0 = tr_read<v_rd_off(1, 0, 0)>(vb), d0 = tr_read<v_rd_off(1, 0, 1)>(vb), c1 = tr_read<v_rd_off(1, 1, 0)>(vb), d1 = tr_read<v_rd_off(1, 1, 1)>(vb);
;     const s16x4 c2 = tr_read<v_rd_off(1, 2, 0)>(vb), d2 = tr_read<v_rd_off(1, 2, 1)>(vb), c3 = tr_read<v_rd_off(1, 3, 0)>(vb), d3 = tr_read<v_rd_off(1, 3, 1)>(vb);
;     asm volatile("s_waitcnt lgkmcnt(8)" ::: "memory"); SBAR();
; DEVI void finishSM(f32x16& p0, f32x16& p1, float alpha, float& l_reg, bf16x8& pa0, bf16x8& pa1, bf16x8& pa2, bf16x8& pa3) {
; #pragma unroll
;     for (int r = 0; r < 16; ++r) p1[r] = __builtin_amdgcn_exp2f(p1[r]);
;     f32x2 s2 = (f32x2){p0[0], p0[1]} + (f32x2){p1[0], p1[1]};
; #pragma unroll
;     for (int r = 2; r < 16; r += 2) s2 += (f32x2){p0[r], p0[r + 1]} + (f32x2){p1[r], p1[r + 1]};
;     float ps = s2[0] + s2[1];
;     { auto rr = __builtin_amdgcn_permlane32_swap(__float_as_uint(ps), __float_as_uint(ps), false, false);
;       ps = __uint_as_float(rr[0]) + __uint_as_float(rr[1]); }
;     l_reg = l_reg * alpha + ps;
;     ...
;     PK4(p0, 0, pa0); PK4(p0, 8, pa1); PK4(p1, 0, pa2); PK4(p1, 8, pa3);
;     ...
; }
	s_waitcnt lgkmcnt(0)
	v_mfma_f32_32x32x16_bf16 v[66:81], v[214:217], v[138:141], v[66:81]
	global_load_lds_dwordx4 v117, s[44:45]
	ds_read_b128 v[210:213], v126
	ds_read_b128 v[214:217], v126 offset:6144
	v_add_u32_e32 v126, s6, v204
	s_waitcnt lgkmcnt(1)
	v_mfma_f32_32x32x16_bf16 v[98:113], v[210:213], v[134:137], v[98:113]
	ds_read_b128 v[210:213], v126
	ds_read_b128 v[218:221], v126 offset:6144
	v_add_u32_e32 v126, s6, v205
	s_waitcnt lgkmcnt(2)
	v_mfma_f32_32x32x16_bf16 v[66:81], v[214:217], v[134:137], v[66:81]
	ds_read_b128 v[214:217], v126
	ds_read_b128 v[222:225], v126 offset:6144
	v_add_u32_e32 v126, s6, v206
	ds_read_b128 v[226:229], v126
	ds_read_b128 v[230:233], v126 offset:6144
	v_add_f32_e32 v126, v50, v82
	v_add_f32_e32 v127, v51, v83
	v_cvt_pk_bf16_f32 v50, v50, v51
	v_cvt_pk_bf16_f32 v51, v52, v53
	s_waitcnt lgkmcnt(5)
	v_mfma_f32_32x32x16_bf16 v[98:113], v[210:213], v[130:133], v[98:113]
	v_add_f32_e64 v210, v52, v84
	v_add_f32_e64 v211, v53, v85
	v_cvt_pk_bf16_f32 v52, v54, v55
	v_cvt_pk_bf16_f32 v53, v56, v57
	v_add_f32_e64 v126, v210, v126
	v_add_f32_e64 v127, v211, v127
	v_add_f32_e64 v210, v54, v86
	v_add_f32_e64 v211, v55, v87
	v_cvt_pk_bf16_f32 v54, v58, v59
	s_waitcnt lgkmcnt(4)
	v_mfma_f32_32x32x16_bf16 v[66:81], v[218:221], v[130:133], v[66:81]
	v_add_f32_e64 v126, v210, v126
	v_add_f32_e64 v127, v211, v127
	v_add_f32_e64 v210, v56, v88
	v_add_f32_e64 v211, v57, v89
	v_cvt_pk_bf16_f32 v55, v60, v61
	v_cvt_pk_bf16_f32 v56, v62, v63
	v_cvt_pk_bf16_f32 v57, v64, v65
	v_add_f32_e64 v126, v210, v126
	v_add_f32_e64 v127, v211, v127
	v_add_f32_e32 v210, v58, v90
	v_add_f32_e32 v211, v59, v91
	v_cvt_pk_bf16_f32 v58, v82, v83
	v_cvt_pk_bf16_f32 v59, v84, v85
	s_waitcnt lgkmcnt(3)
	v_mfma_f32_32x32x16_bf16 v[98:113], v[214:217], v[146:149], v[98:113]
	v_add_f32_e64 v126, v210, v126
	v_add_f32_e64 v127, v211, v127
	v_add_f32_e64 v210, v60, v92
	v_add_f32_e64 v211, v61, v93
	v_cvt_pk_bf16_f32 v60, v86, v87
	v_cvt_pk_bf16_f32 v61, v88, v89
	v_add_f32_e64 v126, v210, v126
	v_add_f32_e64 v127, v211, v127
	v_add_f32_e32 v210, v62, v94
	v_add_f32_e32 v211, v63, v95
	v_cvt_pk_bf16_f32 v62, v90, v91
	v_cvt_pk_bf16_f32 v63, v92, v93
	s_waitcnt lgkmcnt(2)
	v_mfma_f32_32x32x16_bf16 v[66:81], v[222:225], v[146:149], v[66:81]
	v_add_f32_e64 v126, v210, v126
	v_add_f32_e64 v127, v211, v127
	v_add_f32_e64 v210, v64, v96
	v_add_f32_e64 v211, v65, v97
	v_cvt_pk_bf16_f32 v64, v94, v95
	v_cvt_pk_bf16_f32 v65, v96, v97
	ds_read_b64_tr_b16 v[154:155], v202 offset:0x2000
	ds_read_b64_tr_b16 v[156:157], v202 offset:0x2400
	ds_read_b64_tr_b16 v[158:159], v202 offset:0x2800
	ds_read_b64_tr_b16 v[160:161], v202 offset:0x2c00
	ds_read_b64_tr_b16 v[162:163], v202 offset:0x3000
	ds_read_b64_tr_b16 v[164:165], v202 offset:0x3400
	ds_read_b64_tr_b16 v[166:167], v202 offset:0x3800
	ds_read_b64_tr_b16 v[168:169], v202 offset:0x3c00
	v_add_f32_e64 v126, v210, v126
	v_add_f32_e64 v127, v211, v127
	ds_read_b64_tr_b16 v[210:211], v202 offset:0x2200
	ds_read_b64_tr_b16 v[212:213], v202 offset:0x2600
	ds_read_b64_tr_b16 v[214:215], v202 offset:0x2a00
	s_waitcnt lgkmcnt(12)
	v_mfma_f32_32x32x16_bf16 v[98:113], v[226:229], v[142:145], v[98:113]
	ds_read_b64_tr_b16 v[216:217], v202 offset:0x2e00
	ds_read_b64_tr_b16 v[218:219], v202 offset:0x3200
	ds_read_b64_tr_b16 v[220:221], v202 offset:0x3600
	ds_read_b64_tr_b16 v[222:223], v202 offset:0x3a00
	ds_read_b64_tr_b16 v[224:225], v202 offset:0x3e00
	v_add_f32_e32 v126, v126, v127
	s_waitcnt lgkmcnt(15)
	v_mfma_f32_32x32x16_bf16 v[66:81], v[230:233], v[142:145], v[66:81]
	v_mov_b32_e32 v127, v126


; #define SBAR() __builtin_amdgcn_sched_barrier(0)
; DEVI void pv_both(f32x16& o0, f32x16& o1, int vb, bf16x8 pa0, bf16x8 pa1, bf16x8 pa2, bf16x8 pa3) {
;     ...
;     o0 = __builtin_amdgcn_mfma_f32_32x32x16_bf16(pa0, PK(a0, b0), o0, 0, 0, 0);
;     o0 = __builtin_amdgcn_mfma_f32_32x32x16_bf16(pa1, PK(a1, b1), o0, 0, 0, 0);
;     o0 = __builtin_amdgcn_mfma_f32_32x32x16_bf16(pa2, PK(a2, b2), o0, 0, 0, 0);
;     o0 = __builtin_amdgcn_mfma_f32_32x32x16_bf16(pa3, PK(a3, b3), o0, 0, 0, 0);
;     asm volatile("s_waitcnt lgkmcnt(0)" ::: "memory"); SBAR();
;     o1 = __builtin_amdgcn_mfma_f32_32x32x16_bf16(pa0, PK(c0, d0), o1, 0, 0, 0);
;     o1 = __builtin_amdgcn_mfma_f32_32x32x16_bf16(pa1, PK(c1, d1), o1, 0, 0, 0);
;     o1 = __builtin_amdgcn_mfma_f32_32x32x16_bf16(pa2, PK(c2, d2), o1, 0, 0, 0);
;     o1 = __builtin_amdgcn_mfma_f32_32x32x16_bf16(pa3, PK(c3, d3), o1, 0, 0, 0);
;     ...
; }
; template <bool FIRST> DEVI bool partialSM(f32x16& p0, f32x16& p1, float& m_reg, float& alpha) {
;     float pmax = p0[0];
; #pragma unroll
;     for (int r = 1; r < 16; ++r) pmax = fmaxf(pmax, p0[r]);
; #pragma unroll
;     for (int r = 0; r < 16; ++r) pmax = fmaxf(pmax, p1[r]);
;     { auto rr = __builtin_amdgcn_permlane32_swap(__float_as_uint(pmax), __float_as_uint(pmax), false, false);
;       pmax = fmaxf(__uint_as_float(rr[0]), __uint_as_float(rr[1])); }
	s_waitcnt lgkmcnt(14)
	v_mfma_f32_32x32x16_bf16 v[18:33], v[50:53], v[154:157], v[18:33]
	v_permlane32_swap_b32_e32 v126, v127
	s_waitcnt lgkmcnt(6)
	v_mfma_f32_32x32x16_bf16 v[2:17], v[50:53], v[210:213], v[2:17]
	s_nop 1
	v_max_f32_e32 v249, v99, v99
	v_max_f32_e32 v250, v98, v98
	v_max_f32_e32 v249, v250, v249
	v_max3_f32 v249, v249, v100, v101
	v_max3_f32 v249, v249, v102, v103
	v_max3_f32 v251, v249, v104, v105
	v_max3_f32 v251, v251, v106, v107
	v_exp_f32_e32 v50, v98
	v_exp_f32_e32 v51, v99
	v_exp_f32_e32 v52, v100
	v_exp_f32_e32 v53, v101
	v_mfma_f32_32x32x16_bf16 v[18:33], v[54:57], v[158:161], v[18:33]
	s_waitcnt lgkmcnt(4)
	v_mfma_f32_32x32x16_bf16 v[2:17], v[54:57], v[214:217], v[2:17]
	v_max3_f32 v251, v251, v108, v109
	v_max3_f32 v251, v251, v110, v111
	v_max3_f32 v251, v251, v112, v113
	v_max3_f32 v251, v251, v66, v67
	v_max3_f32 v251, v251, v68, v69
	v_max3_f32 v251, v251, v70, v71
	v_max3_f32 v251, v251, v72, v73
	v_exp_f32_e32 v54, v102
	v_exp_f32_e32 v55, v103
	v_exp_f32_e32 v56, v104
	v_exp_f32_e32 v57, v105
	v_mfma_f32_32x32x16_bf16 v[18:33], v[58:61], v[162:165], v[18:33]
	s_waitcnt lgkmcnt(2)
	v_mfma_f32_32x32x16_bf16 v[2:17], v[58:61], v[218:221], v[2:17]
	v_max3_f32 v251, v251, v74, v75
	v_max3_f32 v251, v251, v76, v77
	v_max3_f32 v251, v251, v78, v79
	v_max3_f32 v251, v251, v80, v81
	v_mov_b32_e32 v252, v251


; #define SBAR() __builtin_amdgcn_sched_barrier(0)
; DEVI void pv_both(f32x16& o0, f32x16& o1, int vb, bf16x8 pa0, bf16x8 pa1, bf16x8 pa2, bf16x8 pa3) {
;     ...
;     asm volatile("s_waitcnt lgkmcnt(0)" ::: "memory"); SBAR();
;     o1 = __builtin_amdgcn_mfma_f32_32x32x16_bf16(pa0, PK(c0, d0), o1, 0, 0, 0);
;     o1 = __builtin_amdgcn_mfma_f32_32x32x16_bf16(pa1, PK(c1, d1), o1, 0, 0, 0);
;     o1 = __builtin_amdgcn_mfma_f32_32x32x16_bf16(pa2, PK(c2, d2), o1, 0, 0, 0);
;     o1 = __builtin_amdgcn_mfma_f32_32x32x16_bf16(pa3, PK(c3, d3), o1, 0, 0, 0);
;     ...
; }
; template <bool FIRST> DEVI bool partialSM(f32x16& p0, f32x16& p1, float& m_reg, float& alpha) {
;     float pmax = p0[0];
; #pragma unroll
;     for (int r = 1; r < 16; ++r) pmax = fmaxf(pmax, p0[r]);
; #pragma unroll
;     for (int r = 0; r < 16; ++r) pmax = fmaxf(pmax, p1[r]);
;     { auto rr = __builtin_amdgcn_permlane32_swap(__float_as_uint(pmax), __float_as_uint(pmax), false, false);
;       pmax = fmaxf(__uint_as_float(rr[0]), __uint_as_float(rr[1])); }
;     if (FIRST) { m_reg = pmax; alpha = 1.f;
; #pragma unroll
;         for (int r = 0; r < 16; ++r) { p0[r] = __builtin_amdgcn_exp2f(p0[r] - pmax); p1[r] = p1[r] - pmax; }
;         return false;
;     } else if (__builtin_expect(__all(pmax <= ATT_THR), 1)) { alpha = 1.f;
; #pragma unroll
;         for (int r = 0; r < 16; ++r) p0[r] = __builtin_amdgcn_exp2f(p0[r]);
;         return false;
	v_exp_f32_e32 v58, v106
	v_exp_f32_e32 v59, v107
	v_permlane32_swap_b32_e32 v251, v252
	v_exp_f32_e32 v60, v108
	v_exp_f32_e32 v61, v109
	v_mfma_f32_32x32x16_bf16 v[18:33], v[62:65], v[166:169], v[18:33]
	s_waitcnt lgkmcnt(0)
	v_mfma_f32_32x32x16_bf16 v[2:17], v[62:65], v[222:225], v[2:17]
	v_exp_f32_e32 v62, v110
	v_exp_f32_e32 v63, v111
	v_exp_f32_e32 v64, v112
	v_exp_f32_e32 v65, v113
	v_max_f32_e32 v252, v252, v252
	v_max_f32_e32 v251, v251, v251
	v_max_f32_e32 v174, v251, v252
	v_cmp_ge_f32_e32 vcc, s79, v174
	s_cmp_lg_u64 vcc, exec
	s_cselect_b64 s[6:7], -1, 0
	s_cbranch_scc1 .LBB0_711
	v_mov_b32_e32 v202, 1.0
	v_mov_b32_e32 v203, v209
	s_branch .LBB0_716

; DEVI void cv_finish(char* img  , int lane, const CvRegs& R) {
;     if (!R.live) return;
;     const int n4 = (lane & 7) * 4, kq = lane >> 3;
;     const float sc = R.c.perm ? 16.f : 1.f;
.LBB0_710:
	s_cmp_eq_u32 s95, 0
	s_cselect_b64 vcc, -1, 0
	s_waitcnt vmcnt(0)
	s_cbranch_scc0 .Lmy_cvs_a

; DEVI unsigned cvt_pk_bf16(float lo, float hi) { unsigned r; asm volatile("v_cvt_pk_bf16_f32 %0, %1, %2" : "=v"(r) : "v"(lo), "v"(hi)); return r; }
; DEVI void cv_finish(char* img  , int lane, const CvRegs& R) {
;     ...
;     const float sc = R.c.perm ? 16.f : 1.f;
; #pragma unroll
;     for (int c = 0; c < 4; ++c) { *(unsigned*)(img + (n4 + c) * 68 + (2 * kq) * 2) = cvt_pk_bf16(R.a0[c] * sc, R.b0[c] * sc); *(unsigned*)(img + (n4 + c) * 68 + (2 * kq + 16) * 2) = cvt_pk_bf16(R.a1[c] * sc, R.b1[c] * sc); }
	v_cvt_pk_bf16_f32 v67, v154, v158
	v_cvt_pk_bf16_f32 v69, v162, v166
	ds_write2_b32 v170, v67, v69 offset0:0 offset1:8
	v_cvt_pk_bf16_f32 v67, v155, v159
	v_cvt_pk_bf16_f32 v69, v163, v167
	ds_write2_b32 v170, v67, v69 offset0:17 offset1:25
	v_cvt_pk_bf16_f32 v67, v156, v160
	v_cvt_pk_bf16_f32 v69, v164, v168
	ds_write2_b32 v170, v67, v69 offset0:34 offset1:42
	v_cvt_pk_bf16_f32 v67, v157, v161
	v_cvt_pk_bf16_f32 v69, v165, v169
	ds_write2_b32 v170, v67, v69 offset0:51 offset1:59


; DEVI unsigned cvt_pk_bf16(float lo, float hi) { unsigned r; asm volatile("v_cvt_pk_bf16_f32 %0, %1, %2" : "=v"(r) : "v"(lo), "v"(hi)); return r; }
; DEVI void cv_finish(char* img  , int lane, const CvRegs& R) {
;     ...
;     for (int c = 0; c < 4; ++c) { *(unsigned*)(img + (n4 + c) * 68 + (2 * kq) * 2) = cvt_pk_bf16(R.a0[c] * sc, R.b0[c] * sc); *(unsigned*)(img + (n4 + c) * 68 + (2 * kq + 16) * 2) = cvt_pk_bf16(R.a1[c] * sc, R.b1[c] * sc); }
;     asm volatile("" ::: "memory"); __builtin_amdgcn_wave_barrier();
	s_branch .Lmy_cvj_a

; DEVI void cv_finish(char* img  , int lane, const CvRegs& R) {
;     ...
;     const int n = lane >> 1, half = lane & 1; u32x4 w0, w1;
; #pragma unroll
;     for (int j = 0; j < 4; ++j) { w0[j] = *(const unsigned*)(img + n * 68 + half * 32 + j * 4); w1[j] = *(const unsigned*)(img + n * 68 + half * 32 + 16 + j * 4); }
.Lmy_cvj_a:
	ds_read2_b32 v[66:67], v171 offset1:1
	ds_read2_b32 v[70:71], v171 offset0:4 offset1:5
	ds_read2_b32 v[72:73], v171 offset0:6 offset1:7
	ds_read2_b32 v[68:69], v171 offset0:2 offset1:3


; #define VM0() asm volatile("s_waitcnt vmcnt(0)" ::: "memory")
; DEVI void cv_finish(char* img  , int lane, const CvRegs& R) {
;     ...
;     bf16_t* d = R.c.dst + (size_t)row * R.c.K + R.c.k0 + half * 16;
;     __builtin_nontemporal_store(w0, (u32x4*)d); __builtin_nontemporal_store(w1, (u32x4*)(d + 8));
;     asm volatile("" ::: "memory"); __builtin_amdgcn_wave_barrier();
; DEVI void attn_unit8(const Params& p, char* smem, int unit, int l, int& cvs  , CvRun& crun) {
;     ...
;         if (cvr.live) asm volatile("s_waitcnt vmcnt(2)" ::: "memory"); else VM0();
	s_waitcnt lgkmcnt(0)
	global_store_dwordx4 v246, v[66:69], s[40:41] nt
	global_store_dwordx4 v246, v[70:73], s[40:41] offset:16 nt
	s_waitcnt vmcnt(2)
	s_cbranch_execz .LBB0_701
	s_branch .LBB0_702

; DEVI int tidx() { int t = threadIdx.x; asm volatile("" : "+v"(t)); __builtin_assume(t >= 0 && t < 512); return t; }
; DEVI unsigned cvt_pk_bf16(float lo, float hi) { unsigned r; asm volatile("v_cvt_pk_bf16_f32 %0, %1, %2" : "=v"(r) : "v"(lo), "v"(hi)); return r; }
; DEVI float bf2f(bf16_t h) { return __uint_as_float(((unsigned)h) << 16); }
; DEVI void attn_unit8(const Params& p, char* smem, int unit, int l, int& cvs  , CvRun& crun) {
;     const int tid = tidx(), wid = __builtin_amdgcn_readfirstlane(tid >> 6), lane = tid & 63, r32 = lane & 31, hi = lane >> 5;
;     const int x8 = unit & 7, v8 = unit >> 3, bh = x8 + 8 * (v8 >> 4), qt = v8 & 15, b = bh >> 3, hh = bh & 7;
;     char* K_lds = smem; char* V_lds = smem + 73728;
;     float* wsx = (float*)(smem + 122880) + wid * 64; float* li_l = wsx; float* al_l = wsx + 32;
;     const bf16_t* Kg = p.kfull + (size_t)bh * S_ * 96; const bf16_t* Vg = p.vfull + (size_t)bh * S_ * 64;
;     const size_t qtok = (size_t)b * S_ + qt * 256 + wid * 32 + r32;
;     bf16x8 qr[6];
;     { const bf16_t* qp = p.qbuf + qtok * 768 + hh * 96 + hi * 8;
; #pragma unroll
;       for (int d0 = 0; d0 < 6; ++d0) qr[d0] = *(const bf16x8*)(qp + d0 * 16);
;       const f32x4 c0 = *(const f32x4*)(p.cs + qtok * 16 + hi * 8), c1 = *(const f32x4*)(p.cs + qtok * 16 + hi * 8 + 4);
;       const f32x4 s0 = *(const f32x4*)(p.sn + qtok * 16 + hi * 8), s1 = *(const f32x4*)(p.sn + qtok * 16 + hi * 8 + 4);
;       float o1[8], o2[8];
; #pragma unroll
;       for (int j = 0; j < 8; ++j) { const float x1 = bf2f((bf16_t)qr[4][j]), x2 = bf2f((bf16_t)qr[5][j]); const float cc = j < 4 ? c0[j] : c1[j - 4], ss = j < 4 ? s0[j] : s1[j - 4];
;           o1[j] = x1 * cc - x2 * ss; o2[j] = x2 * cc + x1 * ss; }
;       u32x4 w1, w2;
; #pragma unroll
;       for (int j = 0; j < 4; ++j) { w1[j] = cvt_pk_bf16(o1[2 * j], o1[2 * j + 1]); w2[j] = cvt_pk_bf16(o2[2 * j], o2[2 * j + 1]); }
;       qr[4] = *(bf16x8*)&w1; qr[5] = *(bf16x8*)&w2; }
.LBB0_2229:
	v_mov_b32_e32 v86, v0
	s_ashr_i32 s5, s87, 4
	v_readfirstlane_b32 s4, v86
	s_lshr_b32 s53, s4, 6
	s_and_b32 s52, s5, -8
	s_and_b32 s8, s4, 0x3fffffc0
	s_load_dwordx4 s[4:7], s[24:25], 0x1a0
	s_load_dwordx4 s[12:15], s[24:25], 0x110
	s_and_b32 s92, s87, 7
	s_ashr_i32 s16, s87, 7
	s_lshl_b32 s8, s8, 2
	s_or_b32 s10, s52, s92
	s_add_i32 s93, s8, 0
	s_ashr_i32 s17, s16, 31
	s_lshl_b32 s8, s87, 5
	s_ashr_i32 s11, s10, 31
	s_lshl_b64 s[16:17], s[16:17], 12
	s_and_b32 s8, s8, 0xf00
	s_and_b32 s2, s62, 7
	s_add_i32 s93, s93, 0x1e000
	s_waitcnt lgkmcnt(0)
	v_mov_b32_e32 v2, s4
	v_mov_b32_e32 v3, s5
	s_lshl_b64 s[4:5], s[10:11], 19
	s_or_b32 s8, s16, s8
	s_lshl_b32 s11, s53, 5
	v_and_b32_e32 v176, 31, v86
	s_add_u32 s48, s8, s11
	v_or_b32_e32 v10, s48, v176
	s_addc_u32 s49, s17, 0
	v_mad_u64_u32 v[2:3], s[16:17], v10, s74, v[2:3]
	v_bfe_u32 v187, v86, 5, 1
	v_mad_i32_i24 v3, s49, v181, v3
	s_mul_i32 s8, s92, 0xc0
	v_mov_b32_e32 v11, s49
	v_lshl_add_u64 v[2:3], v[2:3], 0, s[8:9]
	v_lshlrev_b32_e32 v178, 4, v187
	v_mov_b32_e32 v179, v175
	v_lshl_add_u64 v[26:27], v[2:3], 0, v[178:179]
	v_lshlrev_b64 v[10:11], 6, v[10:11]
	global_load_dwordx4 v[2:5], v[26:27], off offset:128
	global_load_dwordx4 v[6:9], v[26:27], off offset:160
	v_lshl_add_u64 v[12:13], s[12:13], 0, v[10:11]
	v_and_b32_e32 v174, 32, v86
	v_lshl_add_u64 v[10:11], s[14:15], 0, v[10:11]
	v_lshl_add_u64 v[22:23], v[12:13], 0, v[174:175]
	v_lshl_add_u64 v[18:19], v[10:11], 0, v[174:175]
	global_load_dwordx4 v[10:13], v[18:19], off
	global_load_dwordx4 v[14:17], v[22:23], off
	s_nop 0
	global_load_dwordx4 v[18:21], v[18:19], off offset:16
	s_nop 0
	global_load_dwordx4 v[22:25], v[22:23], off offset:16
	s_load_dwordx2 s[50:51], s[24:25], 0x1b0
	global_load_dwordx4 v[150:153], v[26:27], off
	global_load_dwordx4 v[138:141], v[26:27], off offset:32
	global_load_dwordx4 v[134:137], v[26:27], off offset:64
	global_load_dwordx4 v[130:133], v[26:27], off offset:96
	s_mul_hi_i32 s8, s10, 0xc0000
	s_mul_i32 s10, s10, 0xc0000
	s_add_u32 s10, s6, s10
	s_addc_u32 s11, s7, s8
	s_lshl_b32 s61, s53, 10
	s_add_i32 s96, s61, 0
	s_waitcnt lgkmcnt(0)
	s_add_u32 s4, s50, s4
	s_mov_b32 m0, s96
	v_lshlrev_b32_e32 v88, 6, v187
	s_addc_u32 s5, s51, s5
	s_add_i32 s97, s76, s61
	v_lshlrev_b32_e32 v90, 2, v86
	v_and_b32_e32 v91, 63, v86
	v_lshlrev_b32_e32 v93, 4, v91
	v_lshlrev_b32_e32 v92, 3, v91
	v_lshlrev_b32_e32 v94, 1, v91
	s_mov_b32 s8, s9
	s_mov_b32 s12, s9
	s_mov_b32 s13, s9
	s_mov_b32 s14, s9
	s_mov_b32 s15, s9
	s_mov_b32 s16, s9
	s_mov_b32 s17, s9
	s_mov_b32 s18, s9
	s_mov_b32 s19, s9
	s_mov_b32 s20, s9
	s_mov_b32 s21, s9
	s_mov_b32 s22, s9
	s_mov_b32 s23, s9
	s_mulk_i32 s53, 0x900
	v_mov_b32_e32 v83, v175
	v_mov_b32_e32 v85, v175
	v_and_b32_e32 v114, 28, v90
	v_lshl_add_u32 v188, v176, 2, s93
	v_mul_u32_u24_e32 v202, 0x44, v114
	v_bfe_u32 v196, v91, 1, 2
	v_mov_b32_e32 v208, 1.0
	s_mov_b32 s71, s9
	v_mov_b32_e32 v189, v175
	s_waitcnt vmcnt(9)
	v_lshlrev_b32_e32 v27, 16, v2
	s_waitcnt vmcnt(8)
	v_lshlrev_b32_e32 v26, 16, v6
	v_and_b32_e32 v33, 0xffff0000, v2
	v_lshlrev_b32_e32 v35, 16, v3
	s_waitcnt vmcnt(7)
	v_mov_b32_e32 v28, v10
	s_waitcnt vmcnt(6)
	v_mov_b32_e32 v29, v14
	v_mov_b32_e32 v36, v12
	v_mov_b32_e32 v37, v16
	v_mov_b32_e32 v38, v16
	v_mov_b32_e32 v39, v12
	v_and_b32_e32 v3, 0xffff0000, v3
	v_and_b32_e32 v2, 0xffff0000, v7
	v_mov_b32_e32 v16, v13
	v_mov_b32_e32 v12, v17
	v_and_b32_e32 v32, 0xffff0000, v6
	v_lshlrev_b32_e32 v34, 16, v7
	v_pk_mul_f32 v[6:7], v[28:29], v[26:27]
	v_pk_mul_f32 v[16:17], v[16:17], v[2:3]
	v_pk_mul_f32 v[2:3], v[12:13], v[2:3]
	v_mov_b32_e32 v30, v14
	v_mov_b32_e32 v31, v10
	v_sub_f32_e32 v12, v7, v6
	v_sub_f32_e32 v16, v17, v16
	v_add_f32_e32 v17, v2, v3
	v_lshlrev_b32_e32 v3, 16, v4
	v_lshlrev_b32_e32 v2, 16, v8
	s_waitcnt vmcnt(5)
	v_mov_b32_e32 v6, v18
	s_waitcnt vmcnt(4)
	v_mov_b32_e32 v7, v22
	v_pk_mul_f32 v[26:27], v[30:31], v[26:27]
	v_pk_mul_f32 v[6:7], v[6:7], v[2:3]
	v_add_f32_e32 v13, v26, v27
	v_sub_f32_e32 v26, v7, v6
	v_mov_b32_e32 v6, v22
	v_mov_b32_e32 v7, v18
	v_pk_mul_f32 v[2:3], v[6:7], v[2:3]
	v_mov_b32_e32 v22, v19
	v_add_f32_e32 v27, v2, v3
	v_and_b32_e32 v3, 0xffff0000, v4
	v_and_b32_e32 v2, 0xffff0000, v8
	v_mov_b32_e32 v18, v23
	v_pk_mul_f32 v[6:7], v[22:23], v[2:3]
	v_pk_mul_f32 v[2:3], v[18:19], v[2:3]
	v_sub_f32_e32 v8, v7, v6
	v_add_f32_e32 v18, v2, v3
	v_lshlrev_b32_e32 v3, 16, v5
	v_lshlrev_b32_e32 v2, 16, v9
	v_mov_b32_e32 v6, v20
	v_mov_b32_e32 v7, v24
	v_pk_mul_f32 v[6:7], v[6:7], v[2:3]
	v_mov_b32_e32 v14, v11
	v_sub_f32_e32 v19, v7, v6
	v_mov_b32_e32 v6, v24
	v_mov_b32_e32 v7, v20
	v_pk_mul_f32 v[2:3], v[6:7], v[2:3]
	v_mov_b32_e32 v24, v21
	v_add_f32_e32 v6, v2, v3
	v_and_b32_e32 v3, 0xffff0000, v5
	v_and_b32_e32 v2, 0xffff0000, v9
	v_mov_b32_e32 v20, v25
	v_mov_b32_e32 v10, v15
	v_pk_mul_f32 v[4:5], v[24:25], v[2:3]
	v_pk_mul_f32 v[2:3], v[20:21], v[2:3]
	v_pk_mul_f32 v[14:15], v[14:15], v[32:33]
	v_pk_mul_f32 v[10:11], v[10:11], v[32:33]
	v_pk_mul_f32 v[28:29], v[36:37], v[34:35]
	v_pk_mul_f32 v[30:31], v[38:39], v[34:35]
	v_add_f32_e32 v2, v2, v3
	v_sub_f32_e32 v14, v15, v14
	v_add_f32_e32 v10, v10, v11
	v_sub_f32_e32 v11, v29, v28
	v_add_f32_e32 v15, v30, v31
	v_sub_f32_e32 v4, v5, v4
	v_cvt_pk_bf16_f32 v146, v12, v14
	v_cvt_pk_bf16_f32 v142, v13, v10
	v_cvt_pk_bf16_f32 v147, v11, v16
	v_cvt_pk_bf16_f32 v143, v15, v17
	v_cvt_pk_bf16_f32 v148, v26, v8
	v_cvt_pk_bf16_f32 v144, v27, v18
	v_cvt_pk_bf16_f32 v149, v19, v4
	v_cvt_pk_bf16_f32 v145, v6, v2
	v_mul_u32_u24_e32 v2, 0xaaab, v86
	v_lshrrev_b32_e32 v3, 19, v2
	v_mul_lo_u16_e32 v4, 12, v3
	v_sub_u16_e32 v4, v86, v4
	v_lshrrev_b32_e32 v2, 21, v2
; #define LAS __attribute__((address_space(3)))
; DEVI int v_rd_base(int lane) { return ((lane & 3) << 3) | (((lane >> 2) & 3) << 6) | (((lane >> 4) & 1) << 5) | (((lane >> 5) & 1) << 8); }
; #define VM0() asm volatile("s_waitcnt vmcnt(0)" ::: "memory")
; DEVI void attn_unit8(const Params& p, char* smem, int unit, int l, int& cvs  , CvRun& crun) {
;     ...
;     int ksrc[3];
; #pragma unroll
;     for (int i = 0; i < 3; ++i) { const int pc = tid + 512 * i, row = pc / 12, ch = (pc % 12) ^ ((row >> 2) & 3); ksrc[i] = row * 192 + ch * 16; }
;     const int vsrc = wid * 1024 + ((lane >> 2) & 7) * 128 + (lane >> 5) * 64 + (lane & 3) * 16;
;     LAS char* const Kl = (LAS char*)K_lds + wid * 1024; LAS char* const Vl = (LAS char*)V_lds + wid * 1024;
;     ...
;     const int vb0 = (int)(uintptr_t)(LAS char*)V_lds + v_rd_base(lane);
;     float m_reg = 0.f, l_reg = 0.f; f32x16 o[2];
; #pragma unroll
;     for (int d = 0; d < 2; ++d)
; #pragma unroll
;         for (int r = 0; r < 16; ++r) o[d][r] = 0.f;
;     f32x16 pA0, pA1, pB0, pB1; float alA, alB; bf16x8 pa0, pa1, pa2, pa3;
;     constexpr int NTILE = S_ / 128;
;     B_DMA(0, 0); B_DMA(1, 1); VM0(); __syncthreads();
	v_bitop3_b32 v2, v2, v4, 3 bitop3:0x6c
	v_mul_u32_u24_e32 v3, 0xc0, v3
	v_lshl_add_u32 v174, v2, 4, v3
	v_or_b32_e32 v2, 0x200, v86
	v_mul_u32_u24_sdwa v3, v2, s75 dst_sel:DWORD dst_unused:UNUSED_PAD src0_sel:WORD_0 src1_sel:DWORD
	v_lshrrev_b32_e32 v4, 19, v3
	v_mul_lo_u16_e32 v5, 12, v4
	v_sub_u16_e32 v2, v2, v5
	v_lshrrev_b32_e32 v3, 21, v3
	v_bitop3_b32 v2, v3, v2, 3 bitop3:0x6c
	v_mul_u32_u24_e32 v3, 0xc0, v4
	v_lshl_add_u32 v82, v2, 4, v3
	v_or_b32_e32 v2, 0x400, v86
	v_mul_u32_u24_sdwa v3, v2, s75 dst_sel:DWORD dst_unused:UNUSED_PAD src0_sel:WORD_0 src1_sel:DWORD
	v_lshrrev_b32_e32 v4, 19, v3
	v_mul_lo_u16_e32 v5, 12, v4
	v_sub_u16_e32 v2, v2, v5
	v_lshrrev_b32_e32 v3, 21, v3
	v_bitop3_b32 v2, v3, v2, 3 bitop3:0x6c
	v_mul_u32_u24_e32 v3, 0xc0, v4
	v_lshl_add_u32 v84, v2, 4, v3
	v_lshlrev_b32_e32 v2, 5, v86
	v_and_b32_e32 v87, 0x380, v2
	v_lshlrev_b32_e32 v3, 4, v86
	global_load_lds_dwordx4 v174, s[10:11]
	s_add_i32 m0, s96, 0x2000
	v_or_b32_e32 v2, v88, v87
	v_and_b32_e32 v89, 48, v3
	global_load_lds_dwordx4 v82, s[10:11]
	s_add_i32 m0, s96, 0x4000
	v_or3_b32 v2, v2, v89, s61
	global_load_lds_dwordx4 v84, s[10:11]
	v_mov_b32_e32 v3, v175
	s_mov_b32 m0, s97
	v_lshl_add_u64 v[4:5], s[4:5], 0, v[2:3]
	global_load_lds_dwordx4 v2, s[4:5]
	s_add_i32 m0, s97, 0x2000
	s_mov_b64 s[72:73], 0x2000
	v_lshl_add_u64 v[2:3], v[4:5], 0, s[72:73]
	s_add_u32 s4, s10, 0x6000
	global_load_lds_dwordx4 v[2:3], off
	s_addc_u32 s5, s11, 0
	s_add_i32 m0, s96, 0x6000
	v_lshl_add_u64 v[2:3], v[4:5], 0, s[44:45]
	global_load_lds_dwordx4 v174, s[4:5]
	s_add_i32 m0, s96, 0x8000
	v_mul_u32_u24_e32 v10, 0xc0, v176
	global_load_lds_dwordx4 v82, s[4:5]
	s_add_i32 m0, s96, 0xa000
	v_and_b32_e32 v11, 48, v90
	global_load_lds_dwordx4 v84, s[4:5]
	s_add_i32 m0, s97, 0x4000
	v_bitop3_b32 v129, v178, v10, v11 bitop3:0xde
	global_load_lds_dwordx4 v[2:3], off
	v_lshl_add_u64 v[2:3], v[4:5], 0, s[42:43]
	s_add_i32 m0, s97, 0x6000
	v_add_u32_e32 v190, 0, v129
	global_load_lds_dwordx4 v[2:3], off
	s_waitcnt vmcnt(0)
	s_waitcnt vmcnt(0) lgkmcnt(0)
	s_barrier
; template <bool FIRST> DEVI bool partialSM(f32x16& p0, f32x16& p1, float& m_reg, float& alpha) {
;     float pmax = p0[0];
; #pragma unroll
;     for (int r = 1; r < 16; ++r) pmax = fmaxf(pmax, p0[r]);
; #pragma unroll
;     for (int r = 0; r < 16; ++r) pmax = fmaxf(pmax, p1[r]);
;     { auto rr = __builtin_amdgcn_permlane32_swap(__float_as_uint(pmax), __float_as_uint(pmax), false, false);
;       pmax = fmaxf(__uint_as_float(rr[0]), __uint_as_float(rr[1])); }
;     if (FIRST) { m_reg = pmax; alpha = 1.f;
; #pragma unroll
;         for (int r = 0; r < 16; ++r) { p0[r] = __builtin_amdgcn_exp2f(p0[r] - pmax); p1[r] = p1[r] - pmax; }
;         return false;
; DEVI void qkt(f32x16& p0, f32x16& p1, const char* Kb, const bf16x8 (&qr)[6], int r32, int hi, const f32x16& cinit) {
; #pragma unroll
;     for (int d0 = 0; d0 < 6; ++d0) { const int cb = (d0 * 16 + hi * 8) * 2;
;         const bf16x8 k0 = *(const bf16x8*)(Kb + KSWZ(r32, cb)), k1 = *(const bf16x8*)(Kb + KSWZ(32 + r32, cb));
;         p0 = __builtin_amdgcn_mfma_f32_32x32x16_bf16(k0, qr[d0], d0 == 0 ? cinit : p0, 0, 0, 0);
;         p1 = __builtin_amdgcn_mfma_f32_32x32x16_bf16(k1, qr[d0], d0 == 0 ? cinit : p1, 0, 0, 0); }
; }
	ds_read_b128 v[2:5], v190
	ds_read_b128 v[6:9], v190 offset:6144
	s_waitcnt lgkmcnt(1)
	v_mfma_f32_32x32x16_bf16 v[34:49], v[2:5], v[150:153], 0
	v_or_b32_e32 v2, 32, v178
	v_bitop3_b32 v184, v2, v10, v11 bitop3:0xde
	v_add_u32_e32 v191, 0, v184
	s_mov_b32 s10, s9
	s_mov_b32 s11, s9
	s_lshl_b32 s84, s54, 5
	s_lshl_b32 s85, s54, 4
	s_waitcnt lgkmcnt(0)
	v_mfma_f32_32x32x16_bf16 v[18:33], v[6:9], v[150:153], 0
	ds_read_b128 v[2:5], v191
	ds_read_b128 v[6:9], v191 offset:6144
	s_lshl_b32 s88, s54, 3
	s_lshl_b32 s70, s54, 1
	v_cmp_gt_u32_e64 s[4:5], 32, v91
	s_waitcnt lgkmcnt(1)
	v_mfma_f32_32x32x16_bf16 v[34:49], v[2:5], v[138:141], v[34:49]
	v_or_b32_e32 v2, 64, v178
	v_xad_u32 v185, v2, v11, v10
	v_add_u32_e32 v192, 0, v185
	s_waitcnt lgkmcnt(0)
	v_mfma_f32_32x32x16_bf16 v[18:33], v[6:9], v[138:141], v[18:33]
	ds_read_b128 v[2:5], v192
	ds_read_b128 v[6:9], v192 offset:6144
	s_waitcnt lgkmcnt(1)
	v_mfma_f32_32x32x16_bf16 v[34:49], v[2:5], v[134:137], v[34:49]
	v_or_b32_e32 v2, 0x60, v178
	v_xad_u32 v205, v2, v11, v10
	v_add_u32_e32 v193, 0, v205
	ds_read_b128 v[2:5], v193
	s_waitcnt lgkmcnt(1)
	v_mfma_f32_32x32x16_bf16 v[18:33], v[6:9], v[134:137], v[18:33]
	ds_read_b128 v[6:9], v193 offset:6144
	s_waitcnt lgkmcnt(1)
	v_mfma_f32_32x32x16_bf16 v[34:49], v[2:5], v[130:133], v[34:49]
	v_and_b32_e32 v2, 0xc0, v93
	v_and_or_b32 v12, v92, 24, v2
	v_or_b32_e32 v2, 0x80, v178
	v_xad_u32 v206, v2, v11, v10
	v_add_u32_e32 v194, 0, v206
	ds_read_b128 v[2:5], v194
	s_waitcnt lgkmcnt(1)
	v_mfma_f32_32x32x16_bf16 v[18:33], v[6:9], v[130:133], v[18:33]
	v_and_b32_e32 v6, 32, v94
	v_and_b32_e32 v7, 0x100, v92
	v_or3_b32 v179, v12, v6, v7
	ds_read_b128 v[6:9], v194 offset:6144
	v_add_u32_e32 v115, s76, v179
	s_waitcnt lgkmcnt(1)
	v_mfma_f32_32x32x16_bf16 v[34:49], v[2:5], v[146:149], v[34:49]
	v_or_b32_e32 v2, 0xa0, v178
	v_xad_u32 v207, v2, v11, v10
	v_add_u32_e32 v195, 0, v207
	ds_read_b128 v[2:5], v195
	ds_read_b128 v[50:53], v195 offset:6144
	s_waitcnt lgkmcnt(2)
	v_mfma_f32_32x32x16_bf16 v[18:33], v[6:9], v[146:149], v[18:33]
	s_waitcnt lgkmcnt(1)
	v_mfma_f32_32x32x16_bf16 v[34:49], v[2:5], v[142:145], v[34:49]
	v_mov_b64_e32 v[2:3], s[8:9]
	v_mov_b64_e32 v[4:5], s[10:11]
	v_mov_b64_e32 v[6:7], s[12:13]
	v_mov_b64_e32 v[8:9], s[14:15]
	v_mov_b64_e32 v[10:11], s[16:17]
	v_mov_b64_e32 v[12:13], s[18:19]
	v_mov_b64_e32 v[14:15], s[20:21]
	s_waitcnt lgkmcnt(0)
	v_mfma_f32_32x32x16_bf16 v[18:33], v[50:53], v[142:145], v[18:33]
	s_nop 2
	v_max_f32_e32 v50, v35, v35
	v_max_f32_e32 v51, v34, v34
	v_max_f32_e32 v50, v51, v50
	v_max3_f32 v50, v50, v36, v37
	v_max3_f32 v50, v50, v38, v39
	v_max3_f32 v50, v50, v40, v41
	v_max3_f32 v50, v50, v42, v43
	v_max3_f32 v50, v50, v44, v45
	v_max3_f32 v50, v50, v46, v47
	v_max3_f32 v50, v50, v48, v49
	v_max3_f32 v50, v50, v18, v19
	v_max3_f32 v50, v50, v20, v21
	v_max3_f32 v50, v50, v22, v23
	v_max3_f32 v50, v50, v24, v25
	v_max3_f32 v50, v50, v26, v27
	v_max3_f32 v50, v50, v28, v29
	v_max3_f32 v50, v50, v30, v31
	v_max3_f32 v50, v50, v32, v33
	v_mov_b32_e32 v51, v50
	s_nop 1
	v_permlane32_swap_b32_e32 v50, v51
	v_max_f32_e32 v51, v51, v51
	v_max_f32_e32 v50, v50, v50
	v_max_f32_e32 v204, v50, v51
	v_sub_f32_e32 v34, v34, v204
	v_exp_f32_e32 v50, v34
	v_sub_f32_e32 v34, v35, v204
	v_exp_f32_e32 v51, v34
	v_sub_f32_e32 v34, v36, v204
	v_exp_f32_e32 v52, v34
	v_sub_f32_e32 v34, v37, v204
	v_exp_f32_e32 v53, v34
	v_sub_f32_e32 v34, v38, v204
	v_exp_f32_e32 v54, v34
	v_sub_f32_e32 v34, v39, v204
	v_exp_f32_e32 v55, v34
	v_sub_f32_e32 v34, v40, v204
	v_exp_f32_e32 v56, v34
	v_sub_f32_e32 v34, v41, v204
	v_exp_f32_e32 v57, v34
	v_sub_f32_e32 v34, v42, v204
	v_mov_b64_e32 v[16:17], s[22:23]
	v_exp_f32_e32 v58, v34
	v_sub_f32_e32 v34, v43, v204
	v_sub_f32_e32 v67, v19, v204
	s_add_i32 s8, s53, 0
	v_bfe_u32 v19, v86, 1, 5
	v_exp_f32_e32 v59, v34
	v_sub_f32_e32 v34, v44, v204
	v_sub_f32_e32 v68, v20, v204
	s_add_i32 s8, s8, 0x1e800
	v_and_b32_e32 v20, 28, v19
	s_or_b32 s10, s52, s2
	v_exp_f32_e32 v60, v34
	v_sub_f32_e32 v34, v45, v204
	v_sub_f32_e32 v69, v21, v204
	v_add_u32_e32 v201, s8, v20
	v_mov_b32_e32 v21, s8
	s_lshl_b32 s8, s54, 10
	s_ashr_i32 s11, s10, 31
	v_exp_f32_e32 v61, v34
	v_sub_f32_e32 v34, v46, v204
	s_add_i32 s89, s8, 0xf7f80000
	s_lshl_b64 s[12:13], s[10:11], 19
	v_exp_f32_e32 v62, v34
	v_sub_f32_e32 v34, v47, v204
	v_sub_f32_e32 v66, v18, v204
	v_lshrrev_b32_e32 v18, 2, v86
	s_add_u32 s12, s50, s12
	v_exp_f32_e32 v63, v34
	v_sub_f32_e32 v34, v48, v204
	v_sub_f32_e32 v70, v22, v204
	v_and_b32_e32 v128, 14, v18
	v_lshrrev_b32_e32 v22, 3, v86
	v_and_b32_e32 v18, 12, v18
	s_addc_u32 s13, s51, s13
	s_mul_i32 s8, s10, 0xc0000
	v_exp_f32_e32 v64, v34
	v_sub_f32_e32 v34, v49, v204
	v_mad_u32_u24 v199, v19, s78, v21
	v_and_b32_e32 v19, 0x80, v92
	v_and_b32_e32 v21, 16, v94
	v_and_b32_e32 v22, 4, v22
	v_and_or_b32 v198, v93, s77, v18
	v_or_b32_e32 v18, s61, v87
	s_mul_hi_i32 s2, s10, 0xc0000
	s_add_u32 s6, s6, s8
	v_exp_f32_e32 v65, v34
	v_or3_b32 v197, v19, v22, v21
	v_or3_b32 v18, v18, v88, v89
	v_mov_b32_e32 v19, v175
	s_addc_u32 s2, s7, s2
	v_and_b32_e32 v20, 1, v86

; DEVI unsigned cvt_pk_bf16(float lo, float hi) { unsigned r; asm volatile("v_cvt_pk_bf16_f32 %0, %1, %2" : "=v"(r) : "v"(lo), "v"(hi)); return r; }
; #define C_SPLAT() do { _Pragma("unroll") for (int _r = 0; _r < 16; ++_r) cinit[_r] = -m_reg; asm volatile("" : "+v"(cinit)); } while (0)
; DEVI void cv_finish(char* img  , int lane, const CvRegs& R) {
;     ...
;     const int n4 = (lane & 7) * 4, kq = lane >> 3;
;     const float sc = R.c.perm ? 16.f : 1.f;
; #pragma unroll
;     for (int c = 0; c < 4; ++c) { *(unsigned*)(img + (n4 + c) * 68 + (2 * kq) * 2) = cvt_pk_bf16(R.a0[c] * sc, R.b0[c] * sc); *(unsigned*)(img + (n4 + c) * 68 + (2 * kq + 16) * 2) = cvt_pk_bf16(R.a1[c] * sc, R.b1[c] * sc); }
;     asm volatile("" ::: "memory"); __builtin_amdgcn_wave_barrier();
;     const int n = lane >> 1, half = lane & 1; u32x4 w0, w1;
; #pragma unroll
;     for (int j = 0; j < 4; ++j) { w0[j] = *(const unsigned*)(img + n * 68 + half * 32 + j * 4); w1[j] = *(const unsigned*)(img + n * 68 + half * 32 + 16 + j * 4); }
; DEVI void attn_unit8(const Params& p, char* smem, int unit, int l, int& cvs  , CvRun& crun) {
;     ...
;     { f32x16 z; _Pragma("unroll") for (int r = 0; r < 16; ++r) z[r] = 0.f;
;       qkt(pA0, pA1, K_lds, qr, r32, hi, z); } partialSM<true>(pA0, pA1, m_reg, alA); C_SPLAT();
;     int s0 = 0, s1 = 1, s2 = 2;
	s_add_u32 s6, s6, 0xc000
	v_xor_b32_e32 v34, 0x80000000, v204
	v_sub_f32_e32 v81, v33, v204
	v_sub_f32_e32 v80, v32, v204
	v_sub_f32_e32 v79, v31, v204
	v_sub_f32_e32 v78, v30, v204
	v_sub_f32_e32 v77, v29, v204
	v_sub_f32_e32 v76, v28, v204
	v_sub_f32_e32 v75, v27, v204
	v_sub_f32_e32 v74, v26, v204
	v_sub_f32_e32 v73, v25, v204
	v_sub_f32_e32 v72, v24, v204
	v_sub_f32_e32 v71, v23, v204
	v_lshlrev_b32_e32 v200, 5, v20
	v_lshlrev_b32_e32 v180, 4, v20
	v_mov_b32_e32 v116, v18
	v_add_u32_e32 v117, 0x2000, v18
	s_addc_u32 s7, s2, 0
	s_add_u32 s44, s12, 0x8000
	s_addc_u32 s45, s13, 0
	v_mov_b64_e32 v[32:33], v[16:17]
	v_mov_b32_e32 v35, v34
	v_mov_b32_e32 v36, v34
	v_mov_b32_e32 v37, v34
	v_mov_b32_e32 v38, v34
	v_mov_b32_e32 v39, v34
	v_mov_b32_e32 v40, v34
	v_mov_b32_e32 v41, v34
	v_mov_b32_e32 v42, v34
	v_mov_b32_e32 v43, v34
	v_mov_b32_e32 v44, v34
	v_mov_b32_e32 v45, v34
	v_mov_b32_e32 v46, v34
	v_mov_b32_e32 v47, v34
	v_mov_b32_e32 v48, v34
	v_mov_b32_e32 v49, v34
	v_mov_b32_e32 v118, v174
	v_mov_b32_e32 v120, v82
	v_mov_b32_e32 v122, v84
	s_mov_b64 s[12:13], s[6:7]
	s_add_u32 s67, s6, 0xb4000
	v_add_u32_e32 v170, v201, v202
	v_add_u32_e32 v171, v199, v200
	v_mov_b64_e32 v[30:31], v[14:15]
	v_mov_b64_e32 v[28:29], v[12:13]
	v_mov_b64_e32 v[26:27], v[10:11]
	v_mov_b64_e32 v[24:25], v[8:9]
	v_mov_b64_e32 v[22:23], v[6:7]
	v_mov_b64_e32 v[20:21], v[4:5]
	v_mov_b64_e32 v[18:19], v[2:3]
	s_mov_b32 s6, 2
	s_mov_b32 s61, 1

; DEVI f32x4 ld_nt(const float* p) { return __builtin_nontemporal_load((const f32x4*)p); }
; DEVI void cv_next(const Params& p, int l, int s, int lane, int stride, CvRun& run) {
;     ...
;     run.c = cv_slice(p, l, s, lane); run.left = 0;
;     if ((stride & 511) == 0) {
;         if (s < NS_W13) { const int e = s >> 9, es = stride >> 9; if (e < NE) { run.left = (NE - 1 - e) / es; run.sstep = (long)es * 1024 * 256; run.dstep = (long)es * 512 * 1024; } }
;         else { const int e = (s - NS_W13) >> 8, es = stride >> 8; if (e < NE) { run.left = (NE - 1 - e) / es; run.sstep = (long)es * 256 * 1024; run.dstep = (long)es * 1024 * 256; } } }
; }
; DEVI void cv_issue(const Params& p, int l, int s, int lane, CvRegs& R, CvRun& run) {
;     R.live = s < NS_SLICES ? 1 : 0;
;     if (R.live) { cv_next(p, l, s, lane, (int)gridDim.x * 8, run); R.c = run.c; const int kq = lane >> 3;
;         const float* sp = R.c.src + (size_t)(R.c.k0 + 2 * kq) * R.c.ld;
;         R.a0 = ld_nt(sp); R.b0 = ld_nt(sp + R.c.ld); R.a1 = ld_nt(sp + (size_t)16 * R.c.ld); R.b1 = ld_nt(sp + (size_t)17 * R.c.ld); }
.LBB0_2259:
	v_add_u32_e32 v252, s10, v128
	s_mov_b64 s[68:69], s[18:19]
	s_mov_b64 s[40:41], s[20:21]
	v_mul_lo_u32 v243, v252, s6
	v_lshlrev_b32_e32 v242, 2, v114
	s_lshl_b32 s72, s6, 2
	s_lshl_b32 s73, s6, 6
	v_lshl_add_u32 v242, v243, 2, v242
	v_add_u32_e32 v243, s72, v242
	v_add_u32_e32 v244, s73, v242
	v_add_u32_e32 v245, s73, v243
	s_cmp_eq_u32 s95, 0
	s_cselect_b64 s[72:73], -1, 0
	v_cndmask_b32_e64 v246, v197, v198, s[72:73]
	v_or_b32_e32 v246, v246, v196
	v_add_u32_e32 v246, s8, v246
	v_mul_lo_u32 v246, v246, s94
	v_add3_u32 v246, v246, v180, s10
	v_lshlrev_b32_e32 v246, 1, v246
	v_mov_b32_e32 v247, 0
	s_ashr_i32 s7, s6, 31
	v_mad_i64_i32 v[252:253], s[16:17], v252, s6, 0
	v_lshl_add_u64 v[252:253], v[252:253], 2, v[250:251]
	s_lshl_b64 s[16:17], s[6:7], 2
	v_lshl_add_u64 v[254:255], v[252:253], 0, s[16:17]
	global_load_dwordx4 v[154:157], v[252:253], off nt
	global_load_dwordx4 v[158:161], v[254:255], off nt
	v_mad_i64_i32 v[252:253], s[18:19], s6, 60, v[254:255]
	v_lshl_add_u64 v[254:255], v[252:253], 0, s[16:17]
	global_load_dwordx4 v[162:165], v[252:253], off nt
	global_load_dwordx4 v[166:169], v[254:255], off nt
	s_mov_b64 s[26:27], s[22:23]
	s_mov_b64 s[28:29], s[50:51]
	s_mov_b32 s56, s11
	s_mov_b32 s55, s95

; DEVI void cv_next(const Params& p, int l, int s, int lane, int stride, CvRun& run) {
;     ...
;     run.c = cv_slice(p, l, s, lane); run.left = 0;
;     if ((stride & 511) == 0) {
;         if (s < NS_W13) { const int e = s >> 9, es = stride >> 9; if (e < NE) { run.left = (NE - 1 - e) / es; run.sstep = (long)es * 1024 * 256; run.dstep = (long)es * 512 * 1024; } }
;         else { const int e = (s - NS_W13) >> 8, es = stride >> 8; if (e < NE) { run.left = (NE - 1 - e) / es; run.sstep = (long)es * 256 * 1024; run.dstep = (long)es * 1024 * 256; } } }
; }
	s_mov_b32 s57, s6
	s_mov_b32 s58, s10
	v_mov_b64_e32 v[172:173], v[182:183]
	s_mov_b32 s59, s94
	s_mov_b32 s60, s8

; DEVI void attn_unit8(const Params& p, char* smem, int unit, int l, int& cvs  , CvRun& crun) {
;     ...
;     for (int T = 0; T + 1 < NTILE; ++T) {
;         const char* Kb = K_lds + s0 * 24576; const int vb = vb0 + s0 * 16384;
;     ...
;         if (T + 2 < NTILE) B_DMA(T + 2, s2);
.LBB0_2266:
	s_mul_i32 s98, s61, 0x6000
	s_add_i32 s98, s96, s98
	s_lshl_b32 s99, s61, 14
	s_add_i32 s99, s97, s99
	s_mul_i32 s6, s2, 0x6000
	s_add_i32 s6, s6, 0
	v_add_u32_e32 v249, s6, v129

; DEVI void qkt(f32x16& p0, f32x16& p1, const char* Kb, const bf16x8 (&qr)[6], int r32, int hi, const f32x16& cinit) {
; #pragma unroll
;     for (int d0 = 0; d0 < 6; ++d0) { const int cb = (d0 * 16 + hi * 8) * 2;
;         const bf16x8 k0 = *(const bf16x8*)(Kb + KSWZ(r32, cb)), k1 = *(const bf16x8*)(Kb + KSWZ(32 + r32, cb));
;         p0 = __builtin_amdgcn_mfma_f32_32x32x16_bf16(k0, qr[d0], d0 == 0 ? cinit : p0, 0, 0, 0);
;         p1 = __builtin_amdgcn_mfma_f32_32x32x16_bf16(k1, qr[d0], d0 == 0 ? cinit : p1, 0, 0, 0); }
; }
	s_mov_b32 m0, s98
	s_barrier
	ds_read_b128 v[234:237], v249
	ds_read_b128 v[212:215], v249 offset:6144
	global_load_lds_dwordx4 v118, s[12:13]
	s_waitcnt lgkmcnt(1)
	v_mfma_f32_32x32x16_bf16 v[98:113], v[234:237], v[150:153], v[34:49]
	s_add_i32 m0, s98, 0x2000

; DEVI void qkt(f32x16& p0, f32x16& p1, const char* Kb, const bf16x8 (&qr)[6], int r32, int hi, const f32x16& cinit) {
; #pragma unroll
;     for (int d0 = 0; d0 < 6; ++d0) { const int cb = (d0 * 16 + hi * 8) * 2;
;         const bf16x8 k0 = *(const bf16x8*)(Kb + KSWZ(r32, cb)), k1 = *(const bf16x8*)(Kb + KSWZ(32 + r32, cb));
;         p0 = __builtin_amdgcn_mfma_f32_32x32x16_bf16(k0, qr[d0], d0 == 0 ? cinit : p0, 0, 0, 0);
;         p1 = __builtin_amdgcn_mfma_f32_32x32x16_bf16(k1, qr[d0], d0 == 0 ? cinit : p1, 0, 0, 0); }
; }
	v_add_u32_e32 v126, s6, v184
	global_load_lds_dwordx4 v120, s[12:13]
	s_waitcnt lgkmcnt(0)
	v_mfma_f32_32x32x16_bf16 v[66:81], v[212:215], v[150:153], v[34:49]
	ds_read_b128 v[212:215], v126
	ds_read_b128 v[216:219], v126 offset:6144
	s_add_i32 m0, s98, 0x4000

; DEVI void qkt(f32x16& p0, f32x16& p1, const char* Kb, const bf16x8 (&qr)[6], int r32, int hi, const f32x16& cinit) {
; #pragma unroll
;     for (int d0 = 0; d0 < 6; ++d0) { const int cb = (d0 * 16 + hi * 8) * 2;
;         const bf16x8 k0 = *(const bf16x8*)(Kb + KSWZ(r32, cb)), k1 = *(const bf16x8*)(Kb + KSWZ(32 + r32, cb));
;         p0 = __builtin_amdgcn_mfma_f32_32x32x16_bf16(k0, qr[d0], d0 == 0 ? cinit : p0, 0, 0, 0);
;         p1 = __builtin_amdgcn_mfma_f32_32x32x16_bf16(k1, qr[d0], d0 == 0 ? cinit : p1, 0, 0, 0); }
; }
	v_add_u32_e32 v126, s6, v185
	global_load_lds_dwordx4 v122, s[12:13]
	s_mov_b32 m0, s99
	s_waitcnt lgkmcnt(1)
	v_mfma_f32_32x32x16_bf16 v[98:113], v[212:215], v[138:141], v[98:113]


	global_load_lds_dwordx4 v116, s[44:45]
	s_add_i32 m0, s99, 0x2000


; template <int OFF> DEVI s16x4 tr_read(int vb) { s16x4 r; asm volatile("ds_read_b64_tr_b16 %0, %1 offset:%2" : "=&v"(r) : "v"(vb), "i"(OFF) : "memory"); return r; }
; #define SBAR() __builtin_amdgcn_sched_barrier(0)
; #define PK4(P, BASE, OUT) do { u32x4 w = {cvt_pk_bf16(P[BASE + 0], P[BASE + 1]), cvt_pk_bf16(P[BASE + 2], P[BASE + 3]), cvt_pk_bf16(P[BASE + 4], P[BASE + 5]), cvt_pk_bf16(P[BASE + 6], P[BASE + 7])}; \
;     OUT = *reinterpret_cast<bf16x8*>(&w); } while (0)
; DEVI void pv_both(f32x16& o0, f32x16& o1, int vb, bf16x8 pa0, bf16x8 pa1, bf16x8 pa2, bf16x8 pa3) {
;     const s16x4 a0 = tr_read<v_rd_off(0, 0, 0)>(vb), b0 = tr_read<v_rd_off(0, 0, 1)>(vb), a1 = tr_read<v_rd_off(0, 1, 0)>(vb), b1 = tr_read<v_rd_off(0, 1, 1)>(vb);
;     const s16x4 a2 = tr_read<v_rd_off(0, 2, 0)>(vb), b2 = tr_read<v_rd_off(0, 2, 1)>(vb), a3 = tr_read<v_rd_off(0, 3, 0)>(vb), b3 = tr_read<v_rd_off(0, 3, 1)>(vb);
;     const s16x4 c0 = tr_read<v_rd_off(1, 0, 0)>(vb), d0 = tr_read<v_rd_off(1, 0, 1)>(vb), c1 = tr_read<v_rd_off(1, 1, 0)>(vb), d1 = tr_read<v_rd_off(1, 1, 1)>(vb);
;     const s16x4 c2 = tr_read<v_rd_off(1, 2, 0)>(vb), d2 = tr_read<v_rd_off(1, 2, 1)>(vb), c3 = tr_read<v_rd_off(1, 3, 0)>(vb), d3 = tr_read<v_rd_off(1, 3, 1)>(vb);
;     asm volatile("s_waitcnt lgkmcnt(8)" ::: "memory"); SBAR();
; DEVI void finishSM(f32x16& p0, f32x16& p1, float alpha, float& l_reg, bf16x8& pa0, bf16x8& pa1, bf16x8& pa2, bf16x8& pa3) {
; #pragma unroll
;     for (int r = 0; r < 16; ++r) p1[r] = __builtin_amdgcn_exp2f(p1[r]);
;     f32x2 s2 = (f32x2){p0[0], p0[1]} + (f32x2){p1[0], p1[1]};
; #pragma unroll
;     for (int r = 2; r < 16; r += 2) s2 += (f32x2){p0[r], p0[r + 1]} + (f32x2){p1[r], p1[r + 1]};
;     float ps = s2[0] + s2[1];
;     { auto rr = __builtin_amdgcn_permlane32_swap(__float_as_uint(ps), __float_as_uint(ps), false, false);
;       ps = __uint_as_float(rr[0]) + __uint_as_float(rr[1]); }
;     l_reg = l_reg * alpha + ps;
;     ...
;     PK4(p0, 0, pa0); PK4(p0, 8, pa1); PK4(p1, 0, pa2); PK4(p1, 8, pa3);
;     ...
; }
	s_waitcnt lgkmcnt(0)
	v_mfma_f32_32x32x16_bf16 v[66:81], v[216:219], v[138:141], v[66:81]
	global_load_lds_dwordx4 v117, s[44:45]
	ds_read_b128 v[212:215], v126
	ds_read_b128 v[216:219], v126 offset:6144
	v_add_u32_e32 v126, s6, v205
	s_waitcnt lgkmcnt(1)
	v_mfma_f32_32x32x16_bf16 v[98:113], v[212:215], v[134:137], v[98:113]
	ds_read_b128 v[212:215], v126
	ds_read_b128 v[220:223], v126 offset:6144
	v_add_u32_e32 v126, s6, v206
	s_waitcnt lgkmcnt(2)
	v_mfma_f32_32x32x16_bf16 v[66:81], v[216:219], v[134:137], v[66:81]
	ds_read_b128 v[216:219], v126
	ds_read_b128 v[224:227], v126 offset:6144
	v_add_u32_e32 v126, s6, v207
	ds_read_b128 v[228:231], v126
	ds_read_b128 v[232:235], v126 offset:6144
	v_add_f32_e32 v126, v50, v82
	v_add_f32_e32 v127, v51, v83
	v_cvt_pk_bf16_f32 v50, v50, v51
	v_cvt_pk_bf16_f32 v51, v52, v53
	s_waitcnt lgkmcnt(5)
	v_mfma_f32_32x32x16_bf16 v[98:113], v[212:215], v[130:133], v[98:113]
	v_add_f32_e64 v212, v52, v84
	v_add_f32_e64 v213, v53, v85
	v_cvt_pk_bf16_f32 v52, v54, v55
	v_cvt_pk_bf16_f32 v53, v56, v57
	v_add_f32_e64 v126, v212, v126
	v_add_f32_e64 v127, v213, v127
	v_add_f32_e64 v212, v54, v86
	v_add_f32_e64 v213, v55, v87
	v_cvt_pk_bf16_f32 v54, v58, v59
	s_waitcnt lgkmcnt(4)
	v_mfma_f32_32x32x16_bf16 v[66:81], v[220:223], v[130:133], v[66:81]
	v_add_f32_e64 v126, v212, v126
	v_add_f32_e64 v127, v213, v127
	v_add_f32_e64 v212, v56, v88
	v_add_f32_e64 v213, v57, v89
	v_cvt_pk_bf16_f32 v55, v60, v61
	v_cvt_pk_bf16_f32 v56, v62, v63
	v_cvt_pk_bf16_f32 v57, v64, v65
	v_add_f32_e64 v126, v212, v126
	v_add_f32_e64 v127, v213, v127
	v_add_f32_e32 v212, v58, v90
	v_add_f32_e32 v213, v59, v91
	v_cvt_pk_bf16_f32 v58, v82, v83
	v_cvt_pk_bf16_f32 v59, v84, v85
	s_waitcnt lgkmcnt(3)
	v_mfma_f32_32x32x16_bf16 v[98:113], v[216:219], v[146:149], v[98:113]
	v_add_f32_e64 v126, v212, v126
	v_add_f32_e64 v127, v213, v127
	v_add_f32_e64 v212, v60, v92
	v_add_f32_e64 v213, v61, v93
	v_cvt_pk_bf16_f32 v60, v86, v87
	v_cvt_pk_bf16_f32 v61, v88, v89
	v_add_f32_e64 v126, v212, v126
	v_add_f32_e64 v127, v213, v127
	v_add_f32_e32 v212, v62, v94
	v_add_f32_e32 v213, v63, v95
	v_cvt_pk_bf16_f32 v62, v90, v91
	v_cvt_pk_bf16_f32 v63, v92, v93
	s_waitcnt lgkmcnt(2)
	v_mfma_f32_32x32x16_bf16 v[66:81], v[224:227], v[146:149], v[66:81]
	v_add_f32_e64 v126, v212, v126
	v_add_f32_e64 v127, v213, v127
	v_add_f32_e64 v212, v64, v96
	v_add_f32_e64 v213, v65, v97
	v_cvt_pk_bf16_f32 v64, v94, v95
	v_cvt_pk_bf16_f32 v65, v96, v97
	ds_read_b64_tr_b16 v[154:155], v203 offset:0x2000
	ds_read_b64_tr_b16 v[156:157], v203 offset:0x2400
	ds_read_b64_tr_b16 v[158:159], v203 offset:0x2800
	ds_read_b64_tr_b16 v[160:161], v203 offset:0x2c00
	ds_read_b64_tr_b16 v[162:163], v203 offset:0x3000
	ds_read_b64_tr_b16 v[164:165], v203 offset:0x3400
	ds_read_b64_tr_b16 v[166:167], v203 offset:0x3800
	ds_read_b64_tr_b16 v[168:169], v203 offset:0x3c00
	v_add_f32_e64 v126, v212, v126
	v_add_f32_e64 v127, v213, v127
	ds_read_b64_tr_b16 v[212:213], v203 offset:0x2200
	ds_read_b64_tr_b16 v[214:215], v203 offset:0x2600
	ds_read_b64_tr_b16 v[216:217], v203 offset:0x2a00
	s_waitcnt lgkmcnt(12)
	v_mfma_f32_32x32x16_bf16 v[98:113], v[228:231], v[142:145], v[98:113]
	ds_read_b64_tr_b16 v[218:219], v203 offset:0x2e00
	ds_read_b64_tr_b16 v[220:221], v203 offset:0x3200
	ds_read_b64_tr_b16 v[222:223], v203 offset:0x3600
	ds_read_b64_tr_b16 v[224:225], v203 offset:0x3a00
	ds_read_b64_tr_b16 v[226:227], v203 offset:0x3e00
	v_add_f32_e32 v126, v126, v127
	s_waitcnt lgkmcnt(15)
	v_mfma_f32_32x32x16_bf16 v[66:81], v[232:235], v[142:145], v[66:81]
	v_mov_b32_e32 v127, v126


; #define SBAR() __builtin_amdgcn_sched_barrier(0)
; DEVI void pv_both(f32x16& o0, f32x16& o1, int vb, bf16x8 pa0, bf16x8 pa1, bf16x8 pa2, bf16x8 pa3) {
;     ...
;     o0 = __builtin_amdgcn_mfma_f32_32x32x16_bf16(pa0, PK(a0, b0), o0, 0, 0, 0);
;     o0 = __builtin_amdgcn_mfma_f32_32x32x16_bf16(pa1, PK(a1, b1), o0, 0, 0, 0);
;     o0 = __builtin_amdgcn_mfma_f32_32x32x16_bf16(pa2, PK(a2, b2), o0, 0, 0, 0);
;     o0 = __builtin_amdgcn_mfma_f32_32x32x16_bf16(pa3, PK(a3, b3), o0, 0, 0, 0);
;     asm volatile("s_waitcnt lgkmcnt(0)" ::: "memory"); SBAR();
;     o1 = __builtin_amdgcn_mfma_f32_32x32x16_bf16(pa0, PK(c0, d0), o1, 0, 0, 0);
;     o1 = __builtin_amdgcn_mfma_f32_32x32x16_bf16(pa1, PK(c1, d1), o1, 0, 0, 0);
;     o1 = __builtin_amdgcn_mfma_f32_32x32x16_bf16(pa2, PK(c2, d2), o1, 0, 0, 0);
;     o1 = __builtin_amdgcn_mfma_f32_32x32x16_bf16(pa3, PK(c3, d3), o1, 0, 0, 0);
;     ...
; }
; template <bool FIRST> DEVI bool partialSM(f32x16& p0, f32x16& p1, float& m_reg, float& alpha) {
;     float pmax = p0[0];
; #pragma unroll
;     for (int r = 1; r < 16; ++r) pmax = fmaxf(pmax, p0[r]);
; #pragma unroll
;     for (int r = 0; r < 16; ++r) pmax = fmaxf(pmax, p1[r]);
;     { auto rr = __builtin_amdgcn_permlane32_swap(__float_as_uint(pmax), __float_as_uint(pmax), false, false);
;       pmax = fmaxf(__uint_as_float(rr[0]), __uint_as_float(rr[1])); }
	s_waitcnt lgkmcnt(14)
	v_mfma_f32_32x32x16_bf16 v[18:33], v[50:53], v[154:157], v[18:33]
	v_permlane32_swap_b32_e32 v126, v127
	s_waitcnt lgkmcnt(6)
	v_mfma_f32_32x32x16_bf16 v[2:17], v[50:53], v[212:215], v[2:17]
	s_nop 1
	v_max_f32_e32 v249, v99, v99
	v_max_f32_e32 v250, v98, v98
	v_max_f32_e32 v249, v250, v249
	v_max3_f32 v249, v249, v100, v101
	v_max3_f32 v249, v249, v102, v103
	v_max3_f32 v251, v249, v104, v105
	v_max3_f32 v251, v251, v106, v107
	v_exp_f32_e32 v50, v98
	v_exp_f32_e32 v51, v99
	v_exp_f32_e32 v52, v100
	v_exp_f32_e32 v53, v101
	v_mfma_f32_32x32x16_bf16 v[18:33], v[54:57], v[158:161], v[18:33]
	s_waitcnt lgkmcnt(4)
	v_mfma_f32_32x32x16_bf16 v[2:17], v[54:57], v[216:219], v[2:17]
	v_max3_f32 v251, v251, v108, v109
	v_max3_f32 v251, v251, v110, v111
	v_max3_f32 v251, v251, v112, v113
	v_max3_f32 v251, v251, v66, v67
	v_max3_f32 v251, v251, v68, v69
	v_max3_f32 v251, v251, v70, v71
	v_max3_f32 v251, v251, v72, v73
	v_exp_f32_e32 v54, v102
	v_exp_f32_e32 v55, v103
	v_exp_f32_e32 v56, v104
	v_exp_f32_e32 v57, v105
	v_mfma_f32_32x32x16_bf16 v[18:33], v[58:61], v[162:165], v[18:33]
	s_waitcnt lgkmcnt(2)
	v_mfma_f32_32x32x16_bf16 v[2:17], v[58:61], v[220:223], v[2:17]
	v_max3_f32 v251, v251, v74, v75
	v_max3_f32 v251, v251, v76, v77
	v_max3_f32 v251, v251, v78, v79
	v_max3_f32 v251, v251, v80, v81
	v_mov_b32_e32 v252, v251


; #define SBAR() __builtin_amdgcn_sched_barrier(0)
; DEVI void pv_both(f32x16& o0, f32x16& o1, int vb, bf16x8 pa0, bf16x8 pa1, bf16x8 pa2, bf16x8 pa3) {
;     ...
;     asm volatile("s_waitcnt lgkmcnt(0)" ::: "memory"); SBAR();
;     o1 = __builtin_amdgcn_mfma_f32_32x32x16_bf16(pa0, PK(c0, d0), o1, 0, 0, 0);
;     o1 = __builtin_amdgcn_mfma_f32_32x32x16_bf16(pa1, PK(c1, d1), o1, 0, 0, 0);
;     o1 = __builtin_amdgcn_mfma_f32_32x32x16_bf16(pa2, PK(c2, d2), o1, 0, 0, 0);
;     o1 = __builtin_amdgcn_mfma_f32_32x32x16_bf16(pa3, PK(c3, d3), o1, 0, 0, 0);
;     ...
; }
; template <bool FIRST> DEVI bool partialSM(f32x16& p0, f32x16& p1, float& m_reg, float& alpha) {
;     float pmax = p0[0];
; #pragma unroll
;     for (int r = 1; r < 16; ++r) pmax = fmaxf(pmax, p0[r]);
; #pragma unroll
;     for (int r = 0; r < 16; ++r) pmax = fmaxf(pmax, p1[r]);
;     { auto rr = __builtin_amdgcn_permlane32_swap(__float_as_uint(pmax), __float_as_uint(pmax), false, false);
;       pmax = fmaxf(__uint_as_float(rr[0]), __uint_as_float(rr[1])); }
;     if (FIRST) { m_reg = pmax; alpha = 1.f;
; #pragma unroll
;         for (int r = 0; r < 16; ++r) { p0[r] = __builtin_amdgcn_exp2f(p0[r] - pmax); p1[r] = p1[r] - pmax; }
;         return false;
;     } else if (__builtin_expect(__all(pmax <= ATT_THR), 1)) { alpha = 1.f;
; #pragma unroll
;         for (int r = 0; r < 16; ++r) p0[r] = __builtin_amdgcn_exp2f(p0[r]);
;         return false;
	v_exp_f32_e32 v58, v106
	v_exp_f32_e32 v59, v107
	v_permlane32_swap_b32_e32 v251, v252
	v_exp_f32_e32 v60, v108
	v_exp_f32_e32 v61, v109
	v_mfma_f32_32x32x16_bf16 v[18:33], v[62:65], v[166:169], v[18:33]
	s_waitcnt lgkmcnt(0)
	v_mfma_f32_32x32x16_bf16 v[2:17], v[62:65], v[224:227], v[2:17]
	v_exp_f32_e32 v62, v110
	v_exp_f32_e32 v63, v111
	v_exp_f32_e32 v64, v112
	v_exp_f32_e32 v65, v113
	v_max_f32_e32 v252, v252, v252
	v_max_f32_e32 v251, v251, v251
	v_max_f32_e32 v174, v251, v252
	v_cmp_ge_f32_e32 vcc, s80, v174
	s_cmp_lg_u64 vcc, exec
	s_cselect_b64 s[6:7], -1, 0
	s_cbranch_scc1 .LBB0_2275
	v_mov_b32_e32 v203, 1.0
	v_mov_b32_e32 v204, v210
	s_branch .LBB0_2280
